# lru_a tile loop: loop-top vmcnt(0) relaxed to vmcnt(8) (does not wait for the previous tile's trailing stores); first tile waits before the loop
# baseline (speedup 1.0000x reference)
; __device__ __forceinline__ void lru_load(const Frame& F, int b, int kb, int nt, LruRaw& R) {
;     const bf16_t* P = (const bf16_t*)(F.R1 + R1_P);
;     const int tk = F.lane & 15, g = F.lane >> 4;
;     const int len = nt < 16 ? CTXL : SEQ, tpos = (nt < 16 ? nt * 16 : (nt - 16) * 16) + tk;
;     const bf16_t* pbase = P + (size_t)((nt < 16 ? b * CTXL : TC + b * SEQ)) * 2048 + 1024 + kb * 64 + g * 16;
;     unsigned okm = 0u;
; #pragma unroll
;     for (int tap = 0; tap < 4; ++tap) { const int tp = tpos + tap - 2; const bool ok = (tp >= 0 && tp < len); const bf16_t* pr = pbase + (size_t)(ok ? tp : tpos) * 2048;
;         okm |= ok ? (1u << tap) : 0u;
;         R.a[tap] = *(const u32x4*)pr; R.b[tap] = *(const u32x4*)(pr + 8); }
;     R.ok = okm;
; __device__ __forceinline__ void ph_lru_a(const Frame& F, int jj) {
;     ...
;         const int nt0 = grp * 48;
;         LruRaw raw; lru_load(F, b, kb, nt0 + F.wave, raw);
.LBB0_463:
	s_or_b64 exec, exec, s[6:7]
	v_readlane_b32 s6, v251, 8
	v_readlane_b32 s7, v251, 9
	s_andn2_b64 vcc, exec, s[6:7]
	s_waitcnt lgkmcnt(0)
	s_barrier
	s_cbranch_vccnz .LBB0_438
	s_mul_i32 s2, s10, 11
	s_sub_i32 s2, s11, s2
	s_mul_i32 s2, s2, 48
	s_add_i32 s6, s2, s75
	s_lshl_b32 s7, s6, 4
	s_cmp_lt_i32 s6, 16
	s_cselect_b32 s17, 0x100, s88
	s_add_i32 s8, s7, 0xffffff00
	s_cmp_lt_i32 s6, 16
	s_cselect_b32 s20, s7, s8
	s_ashr_i32 s7, s13, 5
	s_add_i32 s21, s7, s16
	s_lshl_b32 s24, s21, 13
	s_lshl_b32 s13, s21, 8
	s_or_b32 s16, s24, 0x400
	s_cmp_lt_i32 s6, 16
	s_cselect_b32 s6, s13, s16
	s_ashr_i32 s7, s6, 31
	s_lshl_b64 s[6:7], s[6:7], 12
	s_add_u32 s6, s82, s6
	v_or_b32_e32 v14, s20, v104
	s_addc_u32 s7, s83, s7
	s_lshl_b32 s8, s64, 1
	v_add_u32_e32 v4, 1, v14
	s_add_u32 s6, s6, s8
	v_cmp_lt_i32_e32 vcc, -2, v14
	v_cmp_gt_i32_e64 s[46:47], s17, v4
	s_addc_u32 s7, s7, 0
	s_and_b64 vcc, vcc, s[46:47]
	s_cmp_gt_i32 s20, -1
	v_lshl_add_u64 v[12:13], v[94:95], 1, s[6:7]
	s_cselect_b64 s[6:7], -1, 0
	v_cmp_gt_i32_e64 s[46:47], s17, v14
	s_and_b64 s[6:7], s[6:7], s[46:47]
	v_cmp_lt_i32_e64 s[46:47], 0, v14
	v_cmp_ge_i32_e64 s[48:49], s17, v14
	v_add_u32_e32 v26, -2, v14
	s_and_b64 s[46:47], s[46:47], s[48:49]
	v_cmp_lt_i32_e64 s[48:49], 1, v14
	v_cmp_gt_i32_e64 s[50:51], s17, v26
	v_cndmask_b32_e64 v15, 0, 4, s[6:7]
	v_cndmask_b32_e64 v16, 0, 2, s[46:47]
	s_and_b64 s[48:49], s[48:49], s[50:51]
	v_cndmask_b32_e32 v4, v14, v4, vcc
	v_or_b32_e32 v15, v15, v16
	v_cndmask_b32_e64 v16, 0, 1, s[48:49]
	v_cndmask_b32_e64 v17, 0, 8, vcc
	v_ashrrev_i32_e32 v5, 31, v4
	v_or3_b32 v36, v15, v16, v17
	v_ashrrev_i32_e32 v15, 31, v14
	v_lshlrev_b64 v[4:5], 12, v[4:5]
	v_lshlrev_b64 v[16:17], 12, v[14:15]
	v_lshl_add_u64 v[8:9], v[12:13], 0, v[4:5]
	v_lshl_add_u64 v[20:21], v[12:13], 0, v[16:17]
	global_load_dwordx4 v[4:7], v[8:9], off offset:2064
	s_nop 0
	global_load_dwordx4 v[8:11], v[8:9], off offset:2048
	s_nop 0
	global_load_dwordx4 v[16:19], v[20:21], off offset:2064
	global_load_dwordx4 v[28:31], v[20:21], off offset:2048
	v_subbrev_co_u32_e64 v20, vcc, 0, v14, s[46:47]
	v_ashrrev_i32_e32 v21, 31, v20
	v_cndmask_b32_e64 v14, v14, v26, s[48:49]
	v_lshlrev_b64 v[20:21], 12, v[20:21]
	v_ashrrev_i32_e32 v15, 31, v14
	v_lshl_add_u64 v[24:25], v[12:13], 0, v[20:21]
	v_lshlrev_b64 v[14:15], 12, v[14:15]
	global_load_dwordx4 v[20:23], v[24:25], off offset:2064
	global_load_dwordx4 v[32:35], v[24:25], off offset:2048
	v_lshl_add_u64 v[24:25], v[12:13], 0, v[14:15]
	global_load_dwordx4 v[12:15], v[24:25], off offset:2064
	s_nop 0
	global_load_dwordx4 v[24:27], v[24:25], off offset:2048
	s_mov_b32 s9, s65
	s_or_b32 s17, s24, 0x300
	s_lshl_b32 s6, s64, 2
	v_readlane_b32 s7, v251, 2
	s_add_u32 s6, s7, s6
	v_readlane_b32 s7, v251, 3
	v_lshl_add_u64 v[100:101], v[96:97], 0, s[8:9]
	s_mul_i32 s8, s11, 48
	s_addc_u32 s7, s7, 0
	v_readlane_b32 s14, v251, 4
	s_add_i32 s8, s75, s8
	s_mulk_i32 s10, 0x210
	v_lshl_add_u64 v[38:39], s[64:65], 0, v[0:1]
	s_lshl_b32 s26, s21, 1
	v_readlane_b32 s15, v251, 5
	s_sub_i32 s8, s8, s10
	s_or_b32 s27, s26, 1
	v_lshl_add_u64 v[98:99], v[38:39], 2, s[14:15]
	v_lshl_or_b32 v121, s8, 4, v104
	s_mov_b32 s30, s75
	s_waitcnt vmcnt(0)
	s_branch .LBB0_466

; #define LAS __attribute__((address_space(3)))
; __device__ __forceinline__ void lru_conv(const Frame& F, const LruRaw& R, const LAS float* CT, LAS float* ucb) {
;     const int tk = F.lane & 15, g = F.lane >> 4;
;     float acc[16];
; #pragma unroll
;     for (int q = 0; q < 4; ++q) { const f32x4 c4 = *(const LAS f32x4*)(CT + 4 * 64 + g * 16 + q * 4); acc[q * 4] = c4[0]; acc[q * 4 + 1] = c4[1]; acc[q * 4 + 2] = c4[2]; acc[q * 4 + 3] = c4[3]; }
; #pragma unroll
;     for (int tap = 0; tap < 4; ++tap) { float t0[8], t1[8]; const bool ok = (R.ok >> tap) & 1u; const u32x4 z4 = (u32x4){0u, 0u, 0u, 0u};
;         unpack8(ok ? R.a[tap] : z4, t0); unpack8(ok ? R.b[tap] : z4, t1);
; #pragma unroll
;         for (int q = 0; q < 2; ++q) { const f32x4 w0 = *(const LAS f32x4*)(CT + tap * 64 + g * 16 + q * 4), w1 = *(const LAS f32x4*)(CT + tap * 64 + g * 16 + 8 + q * 4);
; #pragma unroll
;             for (int i = 0; i < 4; ++i) { acc[q * 4 + i] = fmaf(w0[i], t0[q * 4 + i], acc[q * 4 + i]); acc[8 + q * 4 + i] = fmaf(w1[i], t1[q * 4 + i], acc[8 + q * 4 + i]); } } }
; #pragma unroll
;     for (int q = 0; q < 4; ++q) *(LAS f32x4*)(ucb + tk * 68 + g * 16 + q * 4) = (f32x4){acc[q * 4], acc[q * 4 + 1], acc[q * 4 + 2], acc[q * 4 + 3]};
.LBB0_466:
	v_bfe_i32 v145, v36, 0, 1
	ds_read_b128 v[38:41], v107
	ds_read_b128 v[42:45], v107 offset:16
	ds_read_b128 v[46:49], v107 offset:32
	ds_read_b128 v[50:53], v107 offset:48
	s_waitcnt vmcnt(8)
	v_and_b32_e32 v37, v145, v24
	v_and_b32_e32 v103, v145, v12
	ds_read_b128 v[54:57], v108
	ds_read_b128 v[58:61], v108 offset:16
	ds_read_b128 v[62:65], v108 offset:32
	ds_read_b128 v[66:69], v108 offset:48
	v_bfe_i32 v182, v36, 1, 1
	v_bfe_i32 v184, v36, 3, 1
	v_and_b32_sdwa v102, v145, v25 dst_sel:WORD_1 dst_unused:UNUSED_PAD src0_sel:DWORD src1_sel:DWORD
	v_and_b32_e32 v134, v182, v32
	ds_read_b128 v[70:73], v108 offset:256
	ds_read_b128 v[74:77], v108 offset:272
	ds_read_b128 v[78:81], v108 offset:288
	ds_read_b128 v[82:85], v108 offset:304
	v_bfe_i32 v183, v36, 2, 1
	v_and_b32_e32 v6, v184, v6
	v_and_b32_e32 v4, v184, v4
	v_lshlrev_b32_e32 v168, 16, v37
	v_and_b32_e32 v169, 0xffff0000, v37
	v_lshlrev_b32_e32 v190, 16, v103
	v_and_b32_e32 v191, 0xffff0000, v103
	v_bitop3_b32 v103, v145, s91, v25 bitop3:0x80
	v_and_b32_sdwa v154, v182, v33 dst_sel:WORD_1 dst_unused:UNUSED_PAD src0_sel:DWORD src1_sel:DWORD
	v_and_b32_e32 v135, v182, v20
	v_and_b32_e32 v136, v183, v28
	v_and_b32_e32 v137, v183, v16
	ds_read_b128 v[86:89], v108 offset:512
	ds_read_b128 v[122:125], v108 offset:528
	ds_read_b128 v[126:129], v108 offset:544
	ds_read_b128 v[130:133], v108 offset:560
	v_and_b32_sdwa v36, v184, v9 dst_sel:WORD_1 dst_unused:UNUSED_PAD src0_sel:DWORD src1_sel:DWORD
	v_and_b32_e32 v138, v184, v8
	v_and_b32_sdwa v8, v184, v7 dst_sel:WORD_1 dst_unused:UNUSED_PAD src0_sel:DWORD src1_sel:DWORD
	v_and_b32_sdwa v160, v184, v5 dst_sel:WORD_1 dst_unused:UNUSED_PAD src0_sel:DWORD src1_sel:DWORD
	v_lshlrev_b32_e32 v166, 16, v134
	v_and_b32_e32 v167, 0xffff0000, v134
	v_lshlrev_b32_e32 v192, 16, v4
	v_and_b32_e32 v193, 0xffff0000, v4
	v_bitop3_b32 v37, v184, s91, v9 bitop3:0x80
	v_bitop3_b32 v155, v182, s91, v33 bitop3:0x80
	v_bitop3_b32 v161, v184, s91, v5 bitop3:0x80
	v_lshlrev_b32_e32 v208, 16, v6
	v_and_b32_e32 v209, 0xffff0000, v6
	v_bitop3_b32 v9, v184, s91, v7 bitop3:0x80
	s_waitcnt lgkmcnt(11)
	v_pk_fma_f32 v[4:5], v[54:55], v[168:169], v[38:39]
	v_pk_fma_f32 v[6:7], v[56:57], v[102:103], v[40:41]
	v_and_b32_sdwa v156, v183, v29 dst_sel:WORD_1 dst_unused:UNUSED_PAD src0_sel:DWORD src1_sel:DWORD
	v_lshlrev_b32_e32 v162, 16, v138
	v_and_b32_e32 v163, 0xffff0000, v138
	v_lshlrev_b32_e32 v164, 16, v136
	v_and_b32_e32 v165, 0xffff0000, v136
	v_lshlrev_b32_e32 v170, 16, v137
	v_and_b32_e32 v171, 0xffff0000, v137
	v_lshlrev_b32_e32 v172, 16, v135
	v_and_b32_e32 v173, 0xffff0000, v135
	v_bitop3_b32 v157, v183, s91, v29 bitop3:0x80
	ds_read_b128 v[134:137], v108 offset:768
	ds_read_b128 v[138:141], v108 offset:784
	ds_read_b128 v[146:149], v108 offset:800
	ds_read_b128 v[150:153], v108 offset:816
	s_waitcnt lgkmcnt(11)
	v_pk_fma_f32 v[4:5], v[70:71], v[166:167], v[4:5]
	v_pk_fma_f32 v[6:7], v[72:73], v[154:155], v[6:7]
	v_and_b32_e32 v91, v145, v26
	s_waitcnt lgkmcnt(7)
	v_pk_fma_f32 v[4:5], v[86:87], v[164:165], v[4:5]
	v_pk_fma_f32 v[6:7], v[88:89], v[156:157], v[6:7]
	v_and_b32_sdwa v90, v145, v27 dst_sel:WORD_1 dst_unused:UNUSED_PAD src0_sel:DWORD src1_sel:DWORD
	v_and_b32_e32 v34, v182, v34
	v_lshlrev_b32_e32 v200, 16, v91
	v_and_b32_e32 v201, 0xffff0000, v91
	v_bitop3_b32 v91, v145, s91, v27 bitop3:0x80
	s_waitcnt lgkmcnt(3)
	v_pk_fma_f32 v[4:5], v[134:135], v[162:163], v[4:5]
	v_pk_fma_f32 v[6:7], v[136:137], v[36:37], v[6:7]
	v_and_b32_sdwa v142, v145, v13 dst_sel:WORD_1 dst_unused:UNUSED_PAD src0_sel:DWORD src1_sel:DWORD
	v_and_b32_sdwa v12, v182, v35 dst_sel:WORD_1 dst_unused:UNUSED_PAD src0_sel:DWORD src1_sel:DWORD
	v_and_b32_e32 v30, v183, v30
	v_bitop3_b32 v143, v145, s91, v13 bitop3:0x80
	v_lshlrev_b32_e32 v198, 16, v34
	v_and_b32_e32 v199, 0xffff0000, v34
	v_bitop3_b32 v13, v182, s91, v35 bitop3:0x80
	ds_write_b128 v109, v[4:7] offset:36864
	v_pk_fma_f32 v[4:5], v[58:59], v[200:201], v[42:43]
	v_pk_fma_f32 v[6:7], v[60:61], v[90:91], v[44:45]
	v_and_b32_sdwa v32, v182, v21 dst_sel:WORD_1 dst_unused:UNUSED_PAD src0_sel:DWORD src1_sel:DWORD
	v_and_b32_sdwa v20, v183, v31 dst_sel:WORD_1 dst_unused:UNUSED_PAD src0_sel:DWORD src1_sel:DWORD
	v_and_b32_e32 v10, v184, v10
	v_bitop3_b32 v33, v182, s91, v21 bitop3:0x80
	v_lshlrev_b32_e32 v196, 16, v30
	v_and_b32_e32 v197, 0xffff0000, v30
	v_bitop3_b32 v21, v183, s91, v31 bitop3:0x80
	v_pk_fma_f32 v[4:5], v[74:75], v[198:199], v[4:5]
	v_pk_fma_f32 v[6:7], v[76:77], v[12:13], v[6:7]
	v_and_b32_sdwa v158, v183, v17 dst_sel:WORD_1 dst_unused:UNUSED_PAD src0_sel:DWORD src1_sel:DWORD
	v_and_b32_sdwa v16, v184, v11 dst_sel:WORD_1 dst_unused:UNUSED_PAD src0_sel:DWORD src1_sel:DWORD
	v_bitop3_b32 v159, v183, s91, v17 bitop3:0x80
	v_lshlrev_b32_e32 v194, 16, v10
	v_and_b32_e32 v195, 0xffff0000, v10
	v_bitop3_b32 v17, v184, s91, v11 bitop3:0x80
	v_pk_fma_f32 v[4:5], v[122:123], v[196:197], v[4:5]
	v_pk_fma_f32 v[6:7], v[124:125], v[20:21], v[6:7]
	s_waitcnt lgkmcnt(3)
	v_pk_fma_f32 v[4:5], v[138:139], v[194:195], v[4:5]
	v_pk_fma_f32 v[6:7], v[140:141], v[16:17], v[6:7]
	s_mov_b32 s28, s30
	s_add_i32 s29, s2, s30
	ds_write_b128 v109, v[4:7] offset:36880
	v_pk_fma_f32 v[4:5], v[62:63], v[190:191], v[46:47]
	v_pk_fma_f32 v[6:7], v[64:65], v[142:143], v[48:49]
	s_add_i32 s30, s30, 8
	v_pk_fma_f32 v[4:5], v[78:79], v[172:173], v[4:5]
	v_pk_fma_f32 v[6:7], v[80:81], v[32:33], v[6:7]
	s_min_i32 s8, s30, s33
	v_and_b32_e32 v14, v145, v14
	v_pk_fma_f32 v[4:5], v[126:127], v[170:171], v[4:5]
	v_pk_fma_f32 v[6:7], v[128:129], v[158:159], v[6:7]
	s_add_i32 s8, s8, s2
	v_and_b32_sdwa v24, v145, v15 dst_sel:WORD_1 dst_unused:UNUSED_PAD src0_sel:DWORD src1_sel:DWORD
	v_and_b32_e32 v22, v182, v22
	v_lshlrev_b32_e32 v206, 16, v14
	v_and_b32_e32 v207, 0xffff0000, v14
	v_bitop3_b32 v25, v145, s91, v15 bitop3:0x80
	s_waitcnt lgkmcnt(3)
; #define LAS __attribute__((address_space(3)))
; __device__ __forceinline__ void lru_load(const Frame& F, int b, int kb, int nt, LruRaw& R) {
;     const bf16_t* P = (const bf16_t*)(F.R1 + R1_P);
;     const int tk = F.lane & 15, g = F.lane >> 4;
;     const int len = nt < 16 ? CTXL : SEQ, tpos = (nt < 16 ? nt * 16 : (nt - 16) * 16) + tk;
; __device__ __forceinline__ void lru_gates(const Frame& F, LAS bf16_t* Wl, const LAS float* CT, LAS float* ucb, float (&av)[2][4][4], unsigned (&pw)[2][4][4]) {
;     const int tk = F.lane & 15, g = F.lane >> 4;
;     bf16x8 bfr[2];
; #pragma unroll
;     for (int ks = 0; ks < 2; ++ks) { const f32x4 u0 = *(const LAS f32x4*)(ucb + tk * 68 + ks * 32 + g * 8), u1 = *(const LAS f32x4*)(ucb + tk * 68 + ks * 32 + g * 8 + 4);
;         u32x4 w; w.x = cvt_pk_bf16(u0[0], u0[1]); w.y = cvt_pk_bf16(u0[2], u0[3]); w.z = cvt_pk_bf16(u1[0], u1[1]); w.w = cvt_pk_bf16(u1[2], u1[3]); __builtin_memcpy(&bfr[ks], &w, 16); }
; #pragma unroll
;     for (int d = 0; d < 2; ++d)
; #pragma unroll
;         for (int et = 0; et < 4; ++et) {
;             f32x4 ra = (f32x4){0.f, 0.f, 0.f, 0.f}, ri = (f32x4){0.f, 0.f, 0.f, 0.f};
; #pragma unroll
;             for (int ks = 0; ks < 2; ++ks) {
;                 const bf16x8 wa = *(const LAS bf16x8*)(Wl + ((d * 2 + 0) * 64 + et * 16 + tk) * 72 + ks * 32 + g * 8);
;                 const bf16x8 wx = *(const LAS bf16x8*)(Wl + ((d * 2 + 1) * 64 + et * 16 + tk) * 72 + ks * 32 + g * 8);
;                 ra = __builtin_amdgcn_mfma_f32_16x16x32_bf16(wa, bfr[ks], ra, 0, 0, 0);
;                 ri = __builtin_amdgcn_mfma_f32_16x16x32_bf16(wx, bfr[ks], ri, 0, 0, 0);
;             }
;             const f32x4 ba4 = *(const LAS f32x4*)(CT + (5 + 3 * d) * 64 + et * 16 + 4 * g), bx4 = *(const LAS f32x4*)(CT + (6 + 3 * d) * 64 + et * 16 + 4 * g), cs4 = *(const LAS f32x4*)(CT + (7 + 3 * d) * 64 + et * 16 + 4 * g);
;             const f32x4 u4 = *(const LAS f32x4*)(ucb + tk * 68 + et * 16 + 4 * g);
; #pragma unroll
;             for (int i = 0; i < 4; ++i) {
;                 const float r = sigmoidf_(ra[i] + ba4[i]), ig = sigmoidf_(ri[i] + bx4[i]);
;                 const float la = __uint_as_float(cvt_pk_bf16(cs4[i] * r, 0.f) << 16), a = __expf(la);
;                 av[d][et][i] = a; pw[d][et][i] = cvt_pk_bf16(la, __builtin_amdgcn_sqrtf(fmaxf(1.0f - a * a, 0.f)) * ig * u4[i]); }
	v_pk_fma_f32 v[4:5], v[146:147], v[192:193], v[4:5]
	v_pk_fma_f32 v[6:7], v[148:149], v[160:161], v[6:7]
	s_lshl_b32 s9, s8, 4
	v_and_b32_sdwa v26, v182, v23 dst_sel:WORD_1 dst_unused:UNUSED_PAD src0_sel:DWORD src1_sel:DWORD
	v_and_b32_e32 v18, v183, v18
	v_lshlrev_b32_e32 v204, 16, v22
	v_and_b32_e32 v205, 0xffff0000, v22
	v_bitop3_b32 v27, v182, s91, v23 bitop3:0x80
	ds_write_b128 v109, v[4:7] offset:36896
	v_pk_fma_f32 v[4:5], v[66:67], v[206:207], v[50:51]
	v_pk_fma_f32 v[6:7], v[68:69], v[24:25], v[52:53]
	s_add_i32 s10, s9, 0xffffff00
	v_and_b32_sdwa v28, v183, v19 dst_sel:WORD_1 dst_unused:UNUSED_PAD src0_sel:DWORD src1_sel:DWORD
	v_lshlrev_b32_e32 v202, 16, v18
	v_and_b32_e32 v203, 0xffff0000, v18
	v_bitop3_b32 v29, v183, s91, v19 bitop3:0x80
	v_pk_fma_f32 v[4:5], v[82:83], v[204:205], v[4:5]
	v_pk_fma_f32 v[6:7], v[84:85], v[26:27], v[6:7]
	s_cmp_lt_i32 s8, 16
	v_pk_fma_f32 v[4:5], v[130:131], v[202:203], v[4:5]
	v_pk_fma_f32 v[6:7], v[132:133], v[28:29], v[6:7]
	s_cselect_b32 s54, s9, s10
	s_waitcnt lgkmcnt(3)
	v_pk_fma_f32 v[4:5], v[150:151], v[208:209], v[4:5]
	v_pk_fma_f32 v[6:7], v[152:153], v[8:9], v[6:7]
	v_or_b32_e32 v102, s54, v104
	ds_write_b128 v109, v[4:7] offset:36912
	s_cselect_b32 s31, 0x100, s88
	v_add_u32_e32 v6, -2, v102
	v_cmp_lt_i32_e32 vcc, 1, v102
	v_cmp_gt_i32_e64 s[46:47], s31, v6
	s_cselect_b32 s8, s13, s16
	s_and_b64 s[46:47], vcc, s[46:47]
	s_ashr_i32 s9, s8, 31
	v_cndmask_b32_e64 v6, v102, v6, s[46:47]
	s_lshl_b64 s[8:9], s[8:9], 12
	v_ashrrev_i32_e32 v7, 31, v6
	v_lshl_add_u64 v[4:5], v[100:101], 0, s[8:9]
	v_lshlrev_b64 v[6:7], 12, v[6:7]
	v_cmp_lt_i32_e32 vcc, 0, v102
	v_cmp_ge_i32_e64 s[48:49], s31, v102
	v_lshl_add_u64 v[6:7], v[4:5], 0, v[6:7]
	s_and_b64 s[48:49], vcc, s[48:49]
	global_load_dwordx4 v[12:15], v[6:7], off offset:2064
	global_load_dwordx4 v[24:27], v[6:7], off offset:2048
	v_subbrev_co_u32_e64 v6, vcc, 0, v102, s[48:49]
	v_ashrrev_i32_e32 v7, 31, v6
	v_lshlrev_b64 v[6:7], 12, v[6:7]
	v_lshl_add_u64 v[6:7], v[4:5], 0, v[6:7]
	v_ashrrev_i32_e32 v103, 31, v102
	global_load_dwordx4 v[20:23], v[6:7], off offset:2064
	global_load_dwordx4 v[32:35], v[6:7], off offset:2048
	v_lshlrev_b64 v[6:7], 12, v[102:103]
	v_lshl_add_u64 v[6:7], v[4:5], 0, v[6:7]
	global_load_dwordx4 v[16:19], v[6:7], off offset:2064
	global_load_dwordx4 v[28:31], v[6:7], off offset:2048
	v_add_u32_e32 v6, 1, v102
	v_cmp_lt_i32_e32 vcc, -2, v102
	v_cmp_gt_i32_e64 s[50:51], s31, v6
	s_and_b64 s[50:51], vcc, s[50:51]
	ds_read_b128 v[36:39], v110 offset:36864
	ds_read_b128 v[40:43], v110 offset:36880
	v_cndmask_b32_e64 v6, v102, v6, s[50:51]
	v_ashrrev_i32_e32 v7, 31, v6
	v_lshlrev_b64 v[6:7], 12, v[6:7]
	v_lshl_add_u64 v[8:9], v[4:5], 0, v[6:7]
	global_load_dwordx4 v[4:7], v[8:9], off offset:2064
	s_nop 0
	global_load_dwordx4 v[8:11], v[8:9], off offset:2048
	s_waitcnt lgkmcnt(1)
	v_cvt_pk_bf16_f32 v56, v36, v37
	v_cvt_pk_bf16_f32 v57, v38, v39
	s_waitcnt lgkmcnt(0)
	v_cvt_pk_bf16_f32 v58, v40, v41
	v_cvt_pk_bf16_f32 v59, v42, v43
	ds_read_b128 v[36:39], v110 offset:36992
	ds_read_b128 v[40:43], v110 offset:37008
	s_waitcnt lgkmcnt(1)
	v_cvt_pk_bf16_f32 v60, v36, v37
	v_cvt_pk_bf16_f32 v61, v38, v39
	s_waitcnt lgkmcnt(0)
	v_cvt_pk_bf16_f32 v62, v40, v41
	v_cvt_pk_bf16_f32 v63, v42, v43
	ds_read_b128 v[36:39], v114
	ds_read_b128 v[40:43], v114 offset:9216
	ds_read_b128 v[44:47], v113
	ds_read_b128 v[48:51], v114 offset:64
	s_waitcnt lgkmcnt(3)
	v_mfma_f32_16x16x32_bf16 v[36:39], v[36:39], v[56:59], 0
	ds_read_b128 v[52:55], v114 offset:9280
	ds_read_b128 v[64:67], v111
	ds_read_b128 v[68:71], v120 offset:36864
	s_cmp_lt_i32 s29, 16
	s_waitcnt lgkmcnt(3)
	v_mfma_f32_16x16x32_bf16 v[36:39], v[48:51], v[60:63], v[36:39]
	ds_read_b128 v[48:51], v112
	s_cselect_b32 s8, s13, s17
	s_waitcnt lgkmcnt(2)
	s_nop 4
	v_add_f32_e32 v36, v36, v64
	v_mul_f32_e32 v36, 0xbfb8aa3b, v36
	v_exp_f32_e32 v36, v36
	v_mfma_f32_16x16x32_bf16 v[40:43], v[40:43], v[56:59], 0
	v_add_f32_e32 v37, v37, v65
	v_mul_f32_e32 v37, 0xbfb8aa3b, v37
	v_add_f32_e32 v36, 1.0, v36
	v_rcp_f32_e32 v36, v36
	v_mfma_f32_16x16x32_bf16 v[40:43], v[52:55], v[60:63], v[40:43]
	v_exp_f32_e32 v37, v37
	v_add_f32_e32 v38, v38, v66
	v_mul_f32_e32 v36, v44, v36
	v_cvt_pk_bf16_f32 v36, v36, v2
	v_add_f32_e32 v37, 1.0, v37
	v_lshlrev_b32_e32 v44, 16, v36
	s_waitcnt lgkmcnt(0)
	s_nop 1
	v_add_f32_e32 v40, v40, v48
	v_mul_f32_e32 v36, 0x3fb8aa3b, v44
	v_mul_f32_e32 v40, 0xbfb8aa3b, v40
	v_exp_f32_e32 v36, v36
	v_exp_f32_e32 v40, v40
	v_rcp_f32_e32 v37, v37
	v_mul_f32_e32 v38, 0xbfb8aa3b, v38
	v_fma_f32 v48, -v36, v36, 1.0
	v_add_f32_e32 v40, 1.0, v40
	v_max_f32_e32 v48, 0, v48
	v_rcp_f32_e32 v40, v40
	v_sqrt_f32_e32 v48, v48
	v_mul_f32_e32 v37, v45, v37
	v_exp_f32_e32 v38, v38
	v_add_f32_e32 v39, v39, v67
	v_mul_f32_e32 v40, v40, v48
	v_mul_f32_e32 v40, v68, v40
	v_cvt_pk_bf16_f32 v52, v44, v40
	v_add_f32_e32 v40, v41, v49
	v_cvt_pk_bf16_f32 v37, v37, v2
	v_mul_f32_e32 v40, 0xbfb8aa3b, v40
	v_lshlrev_b32_e32 v41, 16, v37
	v_mul_f32_e32 v37, 0x3fb8aa3b, v41
	v_exp_f32_e32 v37, v37
	v_exp_f32_e32 v40, v40
	v_add_f32_e32 v38, 1.0, v38
	v_rcp_f32_e32 v38, v38
	v_fma_f32 v44, -v37, v37, 1.0
	v_add_f32_e32 v40, 1.0, v40
	v_max_f32_e32 v44, 0, v44
	v_rcp_f32_e32 v40, v40
	v_sqrt_f32_e32 v44, v44
	v_mul_f32_e32 v38, v46, v38
	v_mul_f32_e32 v39, 0xbfb8aa3b, v39
	v_exp_f32_e32 v39, v39
	v_mul_f32_e32 v40, v40, v44
	v_mul_f32_e32 v40, v69, v40
	v_cvt_pk_bf16_f32 v53, v41, v40
	v_cvt_pk_bf16_f32 v38, v38, v2
	v_add_f32_e32 v40, v42, v50
	v_lshlrev_b32_e32 v41, 16, v38
	v_mul_f32_e32 v38, 0x3fb8aa3b, v41
	v_mul_f32_e32 v40, 0xbfb8aa3b, v40
	v_exp_f32_e32 v38, v38
	v_exp_f32_e32 v40, v40
	v_add_f32_e32 v39, 1.0, v39
	v_rcp_f32_e32 v39, v39
	v_fma_f32 v42, -v38, v38, 1.0
	v_add_f32_e32 v40, 1.0, v40
	v_max_f32_e32 v42, 0, v42
	v_rcp_f32_e32 v40, v40
	v_sqrt_f32_e32 v42, v42
	v_mul_f32_e32 v39, v47, v39
	v_mul_f32_e32 v40, v40, v42
	v_mul_f32_e32 v40, v70, v40
	v_cvt_pk_bf16_f32 v54, v41, v40
	v_cvt_pk_bf16_f32 v39, v39, v2
	v_add_f32_e32 v40, v43, v51
	v_lshlrev_b32_e32 v41, 16, v39
	v_mul_f32_e32 v39, 0x3fb8aa3b, v41
	v_mul_f32_e32 v40, 0xbfb8aa3b, v40
	v_exp_f32_e32 v39, v39
	v_exp_f32_e32 v40, v40
	v_fma_f32 v42, -v39, v39, 1.0
	v_add_f32_e32 v40, 1.0, v40
	v_max_f32_e32 v42, 0, v42
	v_rcp_f32_e32 v40, v40
	v_sqrt_f32_e32 v42, v42
	s_nop 0
	v_mul_f32_e32 v40, v40, v42
	v_mul_f32_e32 v40, v71, v40
	v_cvt_pk_bf16_f32 v55, v41, v40
	ds_read_b128 v[40:43], v114 offset:2304
	ds_read_b128 v[44:47], v114 offset:11520
	ds_read_b128 v[48:51], v113 offset:64
	ds_read_b128 v[64:67], v114 offset:2368
	s_waitcnt lgkmcnt(3)
; #define LAS __attribute__((address_space(3)))
; __device__ __forceinline__ unsigned cvt_pk_bf16(float lo, float hi) { unsigned r; asm volatile("v_cvt_pk_bf16_f32 %0, %1, %2" : "=v"(r) : "v"(lo), "v"(hi)); return r; }
; __device__ __forceinline__ float sigmoidf_(float x) { return __builtin_amdgcn_rcpf(1.0f + __expf(-x)); }
; __device__ __forceinline__ void lru_gates(const Frame& F, LAS bf16_t* Wl, const LAS float* CT, LAS float* ucb, float (&av)[2][4][4], unsigned (&pw)[2][4][4]) {
;     ...
; #pragma unroll
;     for (int d = 0; d < 2; ++d)
; #pragma unroll
;         for (int et = 0; et < 4; ++et) {
;             f32x4 ra = (f32x4){0.f, 0.f, 0.f, 0.f}, ri = (f32x4){0.f, 0.f, 0.f, 0.f};
; #pragma unroll
;             for (int ks = 0; ks < 2; ++ks) {
;                 const bf16x8 wa = *(const LAS bf16x8*)(Wl + ((d * 2 + 0) * 64 + et * 16 + tk) * 72 + ks * 32 + g * 8);
;                 const bf16x8 wx = *(const LAS bf16x8*)(Wl + ((d * 2 + 1) * 64 + et * 16 + tk) * 72 + ks * 32 + g * 8);
;                 ra = __builtin_amdgcn_mfma_f32_16x16x32_bf16(wa, bfr[ks], ra, 0, 0, 0);
;                 ri = __builtin_amdgcn_mfma_f32_16x16x32_bf16(wx, bfr[ks], ri, 0, 0, 0);
;             }
;             const f32x4 ba4 = *(const LAS f32x4*)(CT + (5 + 3 * d) * 64 + et * 16 + 4 * g), bx4 = *(const LAS f32x4*)(CT + (6 + 3 * d) * 64 + et * 16 + 4 * g), cs4 = *(const LAS f32x4*)(CT + (7 + 3 * d) * 64 + et * 16 + 4 * g);
;             const f32x4 u4 = *(const LAS f32x4*)(ucb + tk * 68 + et * 16 + 4 * g);
; #pragma unroll
;             for (int i = 0; i < 4; ++i) {
;                 const float r = sigmoidf_(ra[i] + ba4[i]), ig = sigmoidf_(ri[i] + bx4[i]);
;                 const float la = __uint_as_float(cvt_pk_bf16(cs4[i] * r, 0.f) << 16), a = __expf(la);
;                 av[d][et][i] = a; pw[d][et][i] = cvt_pk_bf16(la, __builtin_amdgcn_sqrtf(fmaxf(1.0f - a * a, 0.f)) * ig * u4[i]); }
	v_mfma_f32_16x16x32_bf16 v[40:43], v[40:43], v[56:59], 0
	ds_read_b128 v[68:71], v114 offset:11584
	ds_read_b128 v[72:75], v111 offset:64
	ds_read_b128 v[76:79], v120 offset:36928
	s_waitcnt lgkmcnt(3)
	v_mfma_f32_16x16x32_bf16 v[40:43], v[64:67], v[60:63], v[40:43]
	ds_read_b128 v[64:67], v112 offset:64
	v_mfma_f32_16x16x32_bf16 v[44:47], v[44:47], v[56:59], 0
	s_waitcnt lgkmcnt(2)
	s_nop 4
	v_add_f32_e32 v40, v40, v72
	v_mul_f32_e32 v40, 0xbfb8aa3b, v40
	v_exp_f32_e32 v40, v40
	v_mfma_f32_16x16x32_bf16 v[44:47], v[68:71], v[60:63], v[44:47]
	v_add_f32_e32 v41, v41, v73
	v_mul_f32_e32 v41, 0xbfb8aa3b, v41
	v_add_f32_e32 v40, 1.0, v40
	v_rcp_f32_e32 v40, v40
	v_exp_f32_e32 v41, v41
	s_waitcnt lgkmcnt(0)
	s_nop 1
	v_add_f32_e32 v44, v44, v64
	v_mul_f32_e32 v44, 0xbfb8aa3b, v44
	v_mul_f32_e32 v40, v48, v40
	v_cvt_pk_bf16_f32 v40, v40, v2
	v_exp_f32_e32 v44, v44
	v_lshlrev_b32_e32 v48, 16, v40
	v_mul_f32_e32 v40, 0x3fb8aa3b, v48
	v_exp_f32_e32 v40, v40
	v_add_f32_e32 v44, 1.0, v44
	v_rcp_f32_e32 v44, v44
	v_add_f32_e32 v41, 1.0, v41
	v_fma_f32 v64, -v40, v40, 1.0
	v_max_f32_e32 v64, 0, v64
	v_sqrt_f32_e32 v64, v64
	v_rcp_f32_e32 v41, v41
	v_add_f32_e32 v42, v42, v74
	v_mul_f32_e32 v42, 0xbfb8aa3b, v42
	v_mul_f32_e32 v44, v44, v64
	v_mul_f32_e32 v44, v76, v44
	v_mul_f32_e32 v41, v49, v41
	v_cvt_pk_bf16_f32 v68, v48, v44
	v_add_f32_e32 v44, v45, v65
	v_cvt_pk_bf16_f32 v41, v41, v2
	v_mul_f32_e32 v44, 0xbfb8aa3b, v44
	v_lshlrev_b32_e32 v45, 16, v41
	v_mul_f32_e32 v41, 0x3fb8aa3b, v45
	v_exp_f32_e32 v41, v41
	v_exp_f32_e32 v44, v44
	v_exp_f32_e32 v42, v42
	v_add_f32_e32 v43, v43, v75
	v_fma_f32 v48, -v41, v41, 1.0
	v_add_f32_e32 v44, 1.0, v44
	v_max_f32_e32 v48, 0, v48
	v_add_f32_e32 v42, 1.0, v42
	v_rcp_f32_e32 v44, v44
	v_sqrt_f32_e32 v48, v48
	v_rcp_f32_e32 v42, v42
	v_mul_f32_e32 v43, 0xbfb8aa3b, v43
	v_exp_f32_e32 v43, v43
	v_mul_f32_e32 v44, v44, v48
	v_mul_f32_e32 v42, v50, v42
	v_mul_f32_e32 v44, v77, v44
	v_cvt_pk_bf16_f32 v69, v45, v44
	v_cvt_pk_bf16_f32 v42, v42, v2
	v_add_f32_e32 v44, v46, v66
	v_lshlrev_b32_e32 v45, 16, v42
	v_mul_f32_e32 v42, 0x3fb8aa3b, v45
	v_mul_f32_e32 v44, 0xbfb8aa3b, v44
	v_exp_f32_e32 v42, v42
	v_exp_f32_e32 v44, v44
	v_add_f32_e32 v43, 1.0, v43
	v_rcp_f32_e32 v43, v43
	v_fma_f32 v46, -v42, v42, 1.0
	v_add_f32_e32 v44, 1.0, v44
	v_max_f32_e32 v46, 0, v46
	v_rcp_f32_e32 v44, v44
	v_sqrt_f32_e32 v46, v46
	v_mul_f32_e32 v43, v51, v43
	v_mul_f32_e32 v44, v44, v46
	v_mul_f32_e32 v44, v78, v44
	v_cvt_pk_bf16_f32 v70, v45, v44
	v_cvt_pk_bf16_f32 v43, v43, v2
	v_add_f32_e32 v44, v47, v67
	v_lshlrev_b32_e32 v45, 16, v43
	v_mul_f32_e32 v43, 0x3fb8aa3b, v45
	v_mul_f32_e32 v44, 0xbfb8aa3b, v44
	v_exp_f32_e32 v43, v43
	v_exp_f32_e32 v44, v44
	v_fma_f32 v46, -v43, v43, 1.0
	v_add_f32_e32 v44, 1.0, v44
	v_max_f32_e32 v46, 0, v46
	v_rcp_f32_e32 v44, v44
	v_sqrt_f32_e32 v46, v46
	s_nop 0
	v_mul_f32_e32 v44, v44, v46
	v_mul_f32_e32 v44, v79, v44
	v_cvt_pk_bf16_f32 v71, v45, v44
	ds_read_b128 v[44:47], v114 offset:4608
	ds_read_b128 v[48:51], v114 offset:13824
	ds_read_b128 v[64:67], v113 offset:128
	ds_read_b128 v[72:75], v114 offset:4672
	s_waitcnt lgkmcnt(3)
	v_mfma_f32_16x16x32_bf16 v[44:47], v[44:47], v[56:59], 0
	ds_read_b128 v[76:79], v114 offset:13888
	ds_read_b128 v[80:83], v111 offset:128
	ds_read_b128 v[84:87], v120 offset:36992
	s_waitcnt lgkmcnt(3)
	v_mfma_f32_16x16x32_bf16 v[44:47], v[72:75], v[60:63], v[44:47]
	ds_read_b128 v[72:75], v112 offset:128
	v_mfma_f32_16x16x32_bf16 v[48:51], v[48:51], v[56:59], 0
	s_waitcnt lgkmcnt(2)
	s_nop 4
	v_add_f32_e32 v44, v44, v80
	v_mul_f32_e32 v44, 0xbfb8aa3b, v44
	v_exp_f32_e32 v44, v44
	v_mfma_f32_16x16x32_bf16 v[48:51], v[76:79], v[60:63], v[48:51]
	v_add_f32_e32 v45, v45, v81
	v_mul_f32_e32 v45, 0xbfb8aa3b, v45
	v_add_f32_e32 v44, 1.0, v44
	v_rcp_f32_e32 v44, v44
	v_exp_f32_e32 v45, v45
	s_waitcnt lgkmcnt(0)
	s_nop 1
	v_add_f32_e32 v48, v48, v72
	v_mul_f32_e32 v48, 0xbfb8aa3b, v48
	v_mul_f32_e32 v44, v64, v44
	v_cvt_pk_bf16_f32 v44, v44, v2
	v_exp_f32_e32 v48, v48
	v_lshlrev_b32_e32 v64, 16, v44
	v_mul_f32_e32 v44, 0x3fb8aa3b, v64
	v_exp_f32_e32 v44, v44
	v_add_f32_e32 v48, 1.0, v48
	v_rcp_f32_e32 v48, v48
	v_add_f32_e32 v45, 1.0, v45
	v_fma_f32 v72, -v44, v44, 1.0
	v_max_f32_e32 v72, 0, v72
	v_sqrt_f32_e32 v72, v72
	v_rcp_f32_e32 v45, v45
	v_add_f32_e32 v46, v46, v82
	v_mul_f32_e32 v46, 0xbfb8aa3b, v46
	v_mul_f32_e32 v48, v48, v72
	v_mul_f32_e32 v48, v84, v48
	v_mul_f32_e32 v45, v65, v45
	v_cvt_pk_bf16_f32 v72, v64, v48
	v_add_f32_e32 v48, v49, v73
	v_cvt_pk_bf16_f32 v45, v45, v2
	v_mul_f32_e32 v48, 0xbfb8aa3b, v48
	v_lshlrev_b32_e32 v49, 16, v45
	v_mul_f32_e32 v45, 0x3fb8aa3b, v49
	v_exp_f32_e32 v45, v45
	v_exp_f32_e32 v48, v48
	v_exp_f32_e32 v46, v46
	v_add_f32_e32 v47, v47, v83
	v_fma_f32 v64, -v45, v45, 1.0
	v_add_f32_e32 v48, 1.0, v48
	v_max_f32_e32 v64, 0, v64
	v_add_f32_e32 v46, 1.0, v46
	v_rcp_f32_e32 v48, v48
	v_sqrt_f32_e32 v64, v64
	v_rcp_f32_e32 v46, v46
	v_mul_f32_e32 v47, 0xbfb8aa3b, v47
	v_exp_f32_e32 v47, v47
	v_mul_f32_e32 v48, v48, v64
	v_mul_f32_e32 v46, v66, v46
	v_mul_f32_e32 v48, v85, v48
	v_cvt_pk_bf16_f32 v73, v49, v48
	v_cvt_pk_bf16_f32 v46, v46, v2
	v_add_f32_e32 v48, v50, v74
	v_lshlrev_b32_e32 v49, 16, v46
	v_mul_f32_e32 v46, 0x3fb8aa3b, v49
	v_mul_f32_e32 v48, 0xbfb8aa3b, v48
	v_exp_f32_e32 v46, v46
	v_exp_f32_e32 v48, v48
	v_add_f32_e32 v47, 1.0, v47
	v_rcp_f32_e32 v47, v47
	v_fma_f32 v50, -v46, v46, 1.0
	v_add_f32_e32 v48, 1.0, v48
	v_max_f32_e32 v50, 0, v50
	v_rcp_f32_e32 v48, v48
	v_sqrt_f32_e32 v50, v50
	v_mul_f32_e32 v47, v67, v47
	v_mul_f32_e32 v48, v48, v50
	v_mul_f32_e32 v48, v86, v48
	v_cvt_pk_bf16_f32 v74, v49, v48
	v_cvt_pk_bf16_f32 v47, v47, v2
	v_add_f32_e32 v48, v51, v75
	v_lshlrev_b32_e32 v49, 16, v47
	v_mul_f32_e32 v47, 0x3fb8aa3b, v49
	v_mul_f32_e32 v48, 0xbfb8aa3b, v48
	v_exp_f32_e32 v47, v47
	v_exp_f32_e32 v48, v48
	v_fma_f32 v50, -v47, v47, 1.0
	v_add_f32_e32 v48, 1.0, v48
	v_max_f32_e32 v50, 0, v50
	v_rcp_f32_e32 v48, v48
	v_sqrt_f32_e32 v50, v50
	s_nop 0
	v_mul_f32_e32 v48, v48, v50
	v_mul_f32_e32 v48, v87, v48
	v_cvt_pk_bf16_f32 v75, v49, v48
	ds_read_b128 v[48:51], v114 offset:6912
	ds_read_b128 v[64:67], v114 offset:16128
	ds_read_b128 v[76:79], v113 offset:192
	ds_read_b128 v[80:83], v114 offset:6976
	s_waitcnt lgkmcnt(3)
; #define LAS __attribute__((address_space(3)))
; __device__ __forceinline__ unsigned cvt_pk_bf16(float lo, float hi) { unsigned r; asm volatile("v_cvt_pk_bf16_f32 %0, %1, %2" : "=v"(r) : "v"(lo), "v"(hi)); return r; }
; __device__ __forceinline__ float sigmoidf_(float x) { return __builtin_amdgcn_rcpf(1.0f + __expf(-x)); }
; __device__ __forceinline__ void lru_gates(const Frame& F, LAS bf16_t* Wl, const LAS float* CT, LAS float* ucb, float (&av)[2][4][4], unsigned (&pw)[2][4][4]) {
;     ...
; #pragma unroll
;     for (int d = 0; d < 2; ++d)
; #pragma unroll
;         for (int et = 0; et < 4; ++et) {
;             f32x4 ra = (f32x4){0.f, 0.f, 0.f, 0.f}, ri = (f32x4){0.f, 0.f, 0.f, 0.f};
; #pragma unroll
;             for (int ks = 0; ks < 2; ++ks) {
;                 const bf16x8 wa = *(const LAS bf16x8*)(Wl + ((d * 2 + 0) * 64 + et * 16 + tk) * 72 + ks * 32 + g * 8);
;                 const bf16x8 wx = *(const LAS bf16x8*)(Wl + ((d * 2 + 1) * 64 + et * 16 + tk) * 72 + ks * 32 + g * 8);
;                 ra = __builtin_amdgcn_mfma_f32_16x16x32_bf16(wa, bfr[ks], ra, 0, 0, 0);
;                 ri = __builtin_amdgcn_mfma_f32_16x16x32_bf16(wx, bfr[ks], ri, 0, 0, 0);
;             }
;             const f32x4 ba4 = *(const LAS f32x4*)(CT + (5 + 3 * d) * 64 + et * 16 + 4 * g), bx4 = *(const LAS f32x4*)(CT + (6 + 3 * d) * 64 + et * 16 + 4 * g), cs4 = *(const LAS f32x4*)(CT + (7 + 3 * d) * 64 + et * 16 + 4 * g);
;             const f32x4 u4 = *(const LAS f32x4*)(ucb + tk * 68 + et * 16 + 4 * g);
; #pragma unroll
;             for (int i = 0; i < 4; ++i) {
;                 const float r = sigmoidf_(ra[i] + ba4[i]), ig = sigmoidf_(ri[i] + bx4[i]);
;                 const float la = __uint_as_float(cvt_pk_bf16(cs4[i] * r, 0.f) << 16), a = __expf(la);
;                 av[d][et][i] = a; pw[d][et][i] = cvt_pk_bf16(la, __builtin_amdgcn_sqrtf(fmaxf(1.0f - a * a, 0.f)) * ig * u4[i]); }
	v_mfma_f32_16x16x32_bf16 v[48:51], v[48:51], v[56:59], 0
	ds_read_b128 v[84:87], v114 offset:16192
	ds_read_b128 v[88:91], v111 offset:192
	ds_read_b128 v[122:125], v120 offset:37056
	s_waitcnt lgkmcnt(3)
	v_mfma_f32_16x16x32_bf16 v[48:51], v[80:83], v[60:63], v[48:51]
	ds_read_b128 v[80:83], v112 offset:192
	v_mfma_f32_16x16x32_bf16 v[64:67], v[64:67], v[56:59], 0
	s_waitcnt lgkmcnt(2)
	s_nop 4
	v_add_f32_e32 v48, v48, v88
	v_mul_f32_e32 v48, 0xbfb8aa3b, v48
	v_exp_f32_e32 v48, v48
	v_mfma_f32_16x16x32_bf16 v[64:67], v[84:87], v[60:63], v[64:67]
	v_add_f32_e32 v49, v49, v89
	v_mul_f32_e32 v49, 0xbfb8aa3b, v49
	v_add_f32_e32 v48, 1.0, v48
	v_rcp_f32_e32 v48, v48
	v_exp_f32_e32 v49, v49
	s_waitcnt lgkmcnt(0)
	s_nop 1
	v_add_f32_e32 v64, v64, v80
	v_mul_f32_e32 v64, 0xbfb8aa3b, v64
	v_mul_f32_e32 v48, v76, v48
	v_cvt_pk_bf16_f32 v48, v48, v2
	v_exp_f32_e32 v64, v64
	v_lshlrev_b32_e32 v76, 16, v48
	v_mul_f32_e32 v48, 0x3fb8aa3b, v76
	v_exp_f32_e32 v48, v48
	v_add_f32_e32 v64, 1.0, v64
	v_rcp_f32_e32 v64, v64
	v_add_f32_e32 v49, 1.0, v49
	v_fma_f32 v80, -v48, v48, 1.0
	v_max_f32_e32 v80, 0, v80
	v_sqrt_f32_e32 v80, v80
	v_rcp_f32_e32 v49, v49
	v_add_f32_e32 v50, v50, v90
	v_mul_f32_e32 v50, 0xbfb8aa3b, v50
	v_mul_f32_e32 v64, v64, v80
	v_mul_f32_e32 v64, v122, v64
	v_mul_f32_e32 v49, v77, v49
	v_cvt_pk_bf16_f32 v76, v76, v64
	v_add_f32_e32 v64, v65, v81
	v_cvt_pk_bf16_f32 v49, v49, v2
	v_mul_f32_e32 v64, 0xbfb8aa3b, v64
	v_lshlrev_b32_e32 v65, 16, v49
	v_mul_f32_e32 v49, 0x3fb8aa3b, v65
	v_exp_f32_e32 v49, v49
	v_exp_f32_e32 v64, v64
	v_exp_f32_e32 v50, v50
	v_add_f32_e32 v51, v51, v91
	v_fma_f32 v77, -v49, v49, 1.0
	v_add_f32_e32 v64, 1.0, v64
	v_max_f32_e32 v77, 0, v77
	v_add_f32_e32 v50, 1.0, v50
	v_rcp_f32_e32 v64, v64
	v_sqrt_f32_e32 v77, v77
	v_rcp_f32_e32 v50, v50
	v_mul_f32_e32 v51, 0xbfb8aa3b, v51
	v_exp_f32_e32 v51, v51
	v_mul_f32_e32 v64, v64, v77
	v_mul_f32_e32 v50, v78, v50
	v_mul_f32_e32 v64, v123, v64
	v_cvt_pk_bf16_f32 v77, v65, v64
	v_cvt_pk_bf16_f32 v50, v50, v2
	v_add_f32_e32 v64, v66, v82
	v_lshlrev_b32_e32 v65, 16, v50
	v_mul_f32_e32 v50, 0x3fb8aa3b, v65
	v_mul_f32_e32 v64, 0xbfb8aa3b, v64
	v_exp_f32_e32 v50, v50
	v_exp_f32_e32 v64, v64
	v_add_f32_e32 v51, 1.0, v51
	v_rcp_f32_e32 v51, v51
	v_fma_f32 v66, -v50, v50, 1.0
	v_add_f32_e32 v64, 1.0, v64
	v_max_f32_e32 v66, 0, v66
	v_rcp_f32_e32 v64, v64
	v_sqrt_f32_e32 v66, v66
	v_mul_f32_e32 v51, v79, v51
	v_mul_f32_e32 v64, v64, v66
	v_mul_f32_e32 v64, v124, v64
	v_cvt_pk_bf16_f32 v78, v65, v64
	v_cvt_pk_bf16_f32 v51, v51, v2
	v_add_f32_e32 v64, v67, v83
	v_lshlrev_b32_e32 v65, 16, v51
	v_mul_f32_e32 v51, 0x3fb8aa3b, v65
	v_mul_f32_e32 v64, 0xbfb8aa3b, v64
	v_exp_f32_e32 v51, v51
	v_exp_f32_e32 v64, v64
	v_fma_f32 v66, -v51, v51, 1.0
	v_add_f32_e32 v64, 1.0, v64
	v_max_f32_e32 v66, 0, v66
	v_rcp_f32_e32 v64, v64
	v_sqrt_f32_e32 v66, v66
	s_nop 0
	v_mul_f32_e32 v64, v64, v66
	v_mul_f32_e32 v64, v125, v64
	v_cvt_pk_bf16_f32 v79, v65, v64
	ds_read_b128 v[64:67], v114 offset:18432
	ds_read_b128 v[80:83], v114 offset:18496
	s_waitcnt lgkmcnt(1)
	v_mfma_f32_16x16x32_bf16 v[64:67], v[64:67], v[56:59], 0
	ds_read_b128 v[84:87], v114 offset:27648
	ds_read_b128 v[88:91], v114 offset:27712
	ds_read_b128 v[122:125], v115
	s_waitcnt lgkmcnt(3)
	v_mfma_f32_16x16x32_bf16 v[64:67], v[80:83], v[60:63], v[64:67]
	ds_read_b128 v[80:83], v116
	s_waitcnt lgkmcnt(3)
	v_mfma_f32_16x16x32_bf16 v[84:87], v[84:87], v[56:59], 0
	s_waitcnt lgkmcnt(2)
	v_mfma_f32_16x16x32_bf16 v[84:87], v[88:91], v[60:63], v[84:87]
	s_waitcnt lgkmcnt(1)
	s_nop 1
	v_add_f32_e32 v64, v64, v122
	v_mul_f32_e32 v64, 0xbfb8aa3b, v64
	v_exp_f32_e32 v64, v64
	ds_read_b128 v[88:91], v117
	ds_read_b128 v[126:129], v120 offset:36864
	s_waitcnt lgkmcnt(2)
	v_add_f32_e32 v80, v84, v80
	v_mul_f32_e32 v80, 0xbfb8aa3b, v80
	v_add_f32_e32 v64, 1.0, v64
	v_rcp_f32_e32 v64, v64
	v_exp_f32_e32 v80, v80
	v_add_f32_e32 v65, v65, v123
	v_mul_f32_e32 v65, 0xbfb8aa3b, v65
	s_waitcnt lgkmcnt(1)
	v_mul_f32_e32 v64, v88, v64
	v_cvt_pk_bf16_f32 v64, v64, v2
	v_add_f32_e32 v80, 1.0, v80
	v_lshlrev_b32_e32 v64, 16, v64
	v_mul_f32_e32 v84, 0x3fb8aa3b, v64
	v_exp_f32_e32 v103, v84
	v_rcp_f32_e32 v80, v80
	v_exp_f32_e32 v65, v65
	v_add_f32_e32 v66, v66, v124
	v_fma_f32 v84, -v103, v103, 1.0
	v_max_f32_e32 v84, 0, v84
	v_sqrt_f32_e32 v84, v84
	v_mul_f32_e32 v66, 0xbfb8aa3b, v66
	v_exp_f32_e32 v66, v66
	v_add_f32_e32 v67, v67, v125
	v_mul_f32_e32 v80, v80, v84
	s_waitcnt lgkmcnt(0)
	v_mul_f32_e32 v80, v126, v80
	v_cvt_pk_bf16_f32 v80, v64, v80
	v_add_f32_e32 v64, 1.0, v65
	v_rcp_f32_e32 v64, v64
	v_add_f32_e32 v65, v85, v81
	v_mul_f32_e32 v65, 0xbfb8aa3b, v65
	v_exp_f32_e32 v65, v65
	v_mul_f32_e32 v64, v89, v64
	v_cvt_pk_bf16_f32 v64, v64, v2
	v_mul_f32_e32 v67, 0xbfb8aa3b, v67
	v_lshlrev_b32_e32 v64, 16, v64
	v_mul_f32_e32 v81, 0x3fb8aa3b, v64
	v_exp_f32_e32 v122, v81
	v_add_f32_e32 v65, 1.0, v65
	v_rcp_f32_e32 v65, v65
	v_exp_f32_e32 v67, v67
	v_fma_f32 v81, -v122, v122, 1.0
	v_max_f32_e32 v81, 0, v81
	v_sqrt_f32_e32 v81, v81
	s_nop 0
	v_mul_f32_e32 v65, v65, v81
	v_mul_f32_e32 v65, v127, v65
	v_cvt_pk_bf16_f32 v81, v64, v65
	v_add_f32_e32 v64, 1.0, v66
	v_rcp_f32_e32 v64, v64
	v_add_f32_e32 v65, v86, v82
	v_mul_f32_e32 v65, 0xbfb8aa3b, v65
	v_exp_f32_e32 v65, v65
	v_mul_f32_e32 v64, v90, v64
	v_cvt_pk_bf16_f32 v64, v64, v2
	v_add_f32_e32 v65, 1.0, v65
	v_lshlrev_b32_e32 v64, 16, v64
	v_mul_f32_e32 v66, 0x3fb8aa3b, v64
	v_exp_f32_e32 v123, v66
	v_rcp_f32_e32 v65, v65
	v_fma_f32 v66, -v123, v123, 1.0
	v_max_f32_e32 v66, 0, v66
	v_sqrt_f32_e32 v66, v66
	s_nop 0
	v_mul_f32_e32 v65, v65, v66
	v_mul_f32_e32 v65, v128, v65
	v_cvt_pk_bf16_f32 v82, v64, v65
	v_add_f32_e32 v64, 1.0, v67
	v_rcp_f32_e32 v64, v64
	v_add_f32_e32 v65, v87, v83
	v_mul_f32_e32 v65, 0xbfb8aa3b, v65
	v_exp_f32_e32 v65, v65
	v_mul_f32_e32 v64, v91, v64
	v_cvt_pk_bf16_f32 v64, v64, v2
	v_add_f32_e32 v65, 1.0, v65
	v_lshlrev_b32_e32 v64, 16, v64
	v_mul_f32_e32 v66, 0x3fb8aa3b, v64
	v_exp_f32_e32 v124, v66
	v_rcp_f32_e32 v65, v65
	v_fma_f32 v66, -v124, v124, 1.0
	v_max_f32_e32 v66, 0, v66
	v_sqrt_f32_e32 v66, v66
	s_nop 0
	v_mul_f32_e32 v65, v65, v66
	v_mul_f32_e32 v65, v129, v65
	v_cvt_pk_bf16_f32 v83, v64, v65
	ds_read_b128 v[64:67], v114 offset:20736
	ds_read_b128 v[84:87], v114 offset:20800
	s_waitcnt lgkmcnt(1)
; #define LAS __attribute__((address_space(3)))
; __device__ __forceinline__ unsigned cvt_pk_bf16(float lo, float hi) { unsigned r; asm volatile("v_cvt_pk_bf16_f32 %0, %1, %2" : "=v"(r) : "v"(lo), "v"(hi)); return r; }
; __device__ __forceinline__ float sigmoidf_(float x) { return __builtin_amdgcn_rcpf(1.0f + __expf(-x)); }
; __device__ __forceinline__ void lru_gates(const Frame& F, LAS bf16_t* Wl, const LAS float* CT, LAS float* ucb, float (&av)[2][4][4], unsigned (&pw)[2][4][4]) {
;     ...
; #pragma unroll
;     for (int d = 0; d < 2; ++d)
; #pragma unroll
;         for (int et = 0; et < 4; ++et) {
;             f32x4 ra = (f32x4){0.f, 0.f, 0.f, 0.f}, ri = (f32x4){0.f, 0.f, 0.f, 0.f};
; #pragma unroll
;             for (int ks = 0; ks < 2; ++ks) {
;                 const bf16x8 wa = *(const LAS bf16x8*)(Wl + ((d * 2 + 0) * 64 + et * 16 + tk) * 72 + ks * 32 + g * 8);
;                 const bf16x8 wx = *(const LAS bf16x8*)(Wl + ((d * 2 + 1) * 64 + et * 16 + tk) * 72 + ks * 32 + g * 8);
;                 ra = __builtin_amdgcn_mfma_f32_16x16x32_bf16(wa, bfr[ks], ra, 0, 0, 0);
;                 ri = __builtin_amdgcn_mfma_f32_16x16x32_bf16(wx, bfr[ks], ri, 0, 0, 0);
;             }
;             const f32x4 ba4 = *(const LAS f32x4*)(CT + (5 + 3 * d) * 64 + et * 16 + 4 * g), bx4 = *(const LAS f32x4*)(CT + (6 + 3 * d) * 64 + et * 16 + 4 * g), cs4 = *(const LAS f32x4*)(CT + (7 + 3 * d) * 64 + et * 16 + 4 * g);
;             const f32x4 u4 = *(const LAS f32x4*)(ucb + tk * 68 + et * 16 + 4 * g);
; #pragma unroll
;             for (int i = 0; i < 4; ++i) {
;                 const float r = sigmoidf_(ra[i] + ba4[i]), ig = sigmoidf_(ri[i] + bx4[i]);
;                 const float la = __uint_as_float(cvt_pk_bf16(cs4[i] * r, 0.f) << 16), a = __expf(la);
;                 av[d][et][i] = a; pw[d][et][i] = cvt_pk_bf16(la, __builtin_amdgcn_sqrtf(fmaxf(1.0f - a * a, 0.f)) * ig * u4[i]); }
	v_mfma_f32_16x16x32_bf16 v[64:67], v[64:67], v[56:59], 0
	ds_read_b128 v[88:91], v114 offset:29952
	ds_read_b128 v[126:129], v114 offset:30016
	ds_read_b128 v[130:133], v115 offset:64
	s_waitcnt lgkmcnt(3)
	v_mfma_f32_16x16x32_bf16 v[64:67], v[84:87], v[60:63], v[64:67]
	ds_read_b128 v[84:87], v116 offset:64
	s_waitcnt lgkmcnt(3)
	v_mfma_f32_16x16x32_bf16 v[88:91], v[88:91], v[56:59], 0
	s_waitcnt lgkmcnt(2)
	v_mfma_f32_16x16x32_bf16 v[88:91], v[126:129], v[60:63], v[88:91]
	s_waitcnt lgkmcnt(1)
	s_nop 1
	v_add_f32_e32 v64, v64, v130
	v_mul_f32_e32 v64, 0xbfb8aa3b, v64
	v_exp_f32_e32 v64, v64
	ds_read_b128 v[126:129], v117 offset:64
	ds_read_b128 v[134:137], v120 offset:36928
	s_waitcnt lgkmcnt(2)
	v_add_f32_e32 v84, v88, v84
	v_mul_f32_e32 v84, 0xbfb8aa3b, v84
	v_add_f32_e32 v64, 1.0, v64
	v_rcp_f32_e32 v64, v64
	v_exp_f32_e32 v84, v84
	v_add_f32_e32 v65, v65, v131
	v_mul_f32_e32 v65, 0xbfb8aa3b, v65
	s_waitcnt lgkmcnt(1)
	v_mul_f32_e32 v64, v126, v64
	v_cvt_pk_bf16_f32 v64, v64, v2
	v_add_f32_e32 v84, 1.0, v84
	v_lshlrev_b32_e32 v64, 16, v64
	v_mul_f32_e32 v88, 0x3fb8aa3b, v64
	v_exp_f32_e32 v125, v88
	v_rcp_f32_e32 v84, v84
	v_exp_f32_e32 v65, v65
	v_add_f32_e32 v66, v66, v132
	v_fma_f32 v88, -v125, v125, 1.0
	v_max_f32_e32 v88, 0, v88
	v_sqrt_f32_e32 v88, v88
	v_mul_f32_e32 v66, 0xbfb8aa3b, v66
	v_exp_f32_e32 v66, v66
	v_add_f32_e32 v67, v67, v133
	v_mul_f32_e32 v84, v84, v88
	s_waitcnt lgkmcnt(0)
	v_mul_f32_e32 v84, v134, v84
	v_cvt_pk_bf16_f32 v84, v64, v84
	v_add_f32_e32 v64, 1.0, v65
	v_rcp_f32_e32 v64, v64
	v_add_f32_e32 v65, v89, v85
	v_mul_f32_e32 v65, 0xbfb8aa3b, v65
	v_exp_f32_e32 v65, v65
	v_mul_f32_e32 v64, v127, v64
	v_cvt_pk_bf16_f32 v64, v64, v2
	v_mul_f32_e32 v67, 0xbfb8aa3b, v67
	v_lshlrev_b32_e32 v64, 16, v64
	v_mul_f32_e32 v85, 0x3fb8aa3b, v64
	v_exp_f32_e32 v126, v85
	v_add_f32_e32 v65, 1.0, v65
	v_rcp_f32_e32 v65, v65
	v_exp_f32_e32 v67, v67
	v_fma_f32 v85, -v126, v126, 1.0
	v_max_f32_e32 v85, 0, v85
	v_sqrt_f32_e32 v85, v85
	s_nop 0
	v_mul_f32_e32 v65, v65, v85
	v_mul_f32_e32 v65, v135, v65
	v_cvt_pk_bf16_f32 v85, v64, v65
	v_add_f32_e32 v64, 1.0, v66
	v_rcp_f32_e32 v64, v64
	v_add_f32_e32 v65, v90, v86
	v_mul_f32_e32 v65, 0xbfb8aa3b, v65
	v_exp_f32_e32 v65, v65
	v_mul_f32_e32 v64, v128, v64
	v_cvt_pk_bf16_f32 v64, v64, v2
	v_add_f32_e32 v65, 1.0, v65
	v_lshlrev_b32_e32 v64, 16, v64
	v_mul_f32_e32 v66, 0x3fb8aa3b, v64
	v_exp_f32_e32 v127, v66
	v_rcp_f32_e32 v65, v65
	v_fma_f32 v66, -v127, v127, 1.0
	v_max_f32_e32 v66, 0, v66
	v_sqrt_f32_e32 v66, v66
	s_nop 0
	v_mul_f32_e32 v65, v65, v66
	v_mul_f32_e32 v65, v136, v65
	v_cvt_pk_bf16_f32 v86, v64, v65
	v_add_f32_e32 v64, 1.0, v67
	v_rcp_f32_e32 v64, v64
	v_add_f32_e32 v65, v91, v87
	v_mul_f32_e32 v65, 0xbfb8aa3b, v65
	v_exp_f32_e32 v65, v65
	v_mul_f32_e32 v64, v129, v64
	v_cvt_pk_bf16_f32 v64, v64, v2
	v_add_f32_e32 v65, 1.0, v65
	v_lshlrev_b32_e32 v64, 16, v64
	v_mul_f32_e32 v66, 0x3fb8aa3b, v64
	v_exp_f32_e32 v128, v66
	v_rcp_f32_e32 v65, v65
	v_fma_f32 v66, -v128, v128, 1.0
	v_max_f32_e32 v66, 0, v66
	v_sqrt_f32_e32 v66, v66
	s_nop 0
	v_mul_f32_e32 v65, v65, v66
	v_mul_f32_e32 v65, v137, v65
	v_cvt_pk_bf16_f32 v87, v64, v65
	ds_read_b128 v[64:67], v114 offset:23040
	ds_read_b128 v[88:91], v114 offset:23104
	s_waitcnt lgkmcnt(1)
	v_mfma_f32_16x16x32_bf16 v[64:67], v[64:67], v[56:59], 0
	ds_read_b128 v[130:133], v114 offset:32256
	ds_read_b128 v[134:137], v114 offset:32320
	ds_read_b128 v[138:141], v115 offset:128
	s_waitcnt lgkmcnt(3)
	v_mfma_f32_16x16x32_bf16 v[64:67], v[88:91], v[60:63], v[64:67]
	ds_read_b128 v[88:91], v116 offset:128
	s_waitcnt lgkmcnt(3)
	v_mfma_f32_16x16x32_bf16 v[130:133], v[130:133], v[56:59], 0
	s_waitcnt lgkmcnt(2)
	v_mfma_f32_16x16x32_bf16 v[130:133], v[134:137], v[60:63], v[130:133]
	s_waitcnt lgkmcnt(1)
	s_nop 1
	v_add_f32_e32 v64, v64, v138
	v_mul_f32_e32 v64, 0xbfb8aa3b, v64
	v_exp_f32_e32 v64, v64
	ds_read_b128 v[134:137], v117 offset:128
	ds_read_b128 v[146:149], v120 offset:36992
	s_waitcnt lgkmcnt(2)
	v_add_f32_e32 v88, v130, v88
	v_mul_f32_e32 v88, 0xbfb8aa3b, v88
	v_add_f32_e32 v64, 1.0, v64
	v_rcp_f32_e32 v64, v64
	v_exp_f32_e32 v88, v88
	v_add_f32_e32 v65, v65, v139
	v_mul_f32_e32 v65, 0xbfb8aa3b, v65
	s_waitcnt lgkmcnt(1)
	v_mul_f32_e32 v64, v134, v64
	v_cvt_pk_bf16_f32 v64, v64, v2
	v_add_f32_e32 v88, 1.0, v88
	v_lshlrev_b32_e32 v64, 16, v64
	v_mul_f32_e32 v129, 0x3fb8aa3b, v64
	v_exp_f32_e32 v129, v129
	v_rcp_f32_e32 v88, v88
	v_exp_f32_e32 v65, v65
	v_add_f32_e32 v66, v66, v140
	v_fma_f32 v130, -v129, v129, 1.0
	v_max_f32_e32 v130, 0, v130
	v_sqrt_f32_e32 v130, v130
	v_mul_f32_e32 v66, 0xbfb8aa3b, v66
	v_exp_f32_e32 v66, v66
	v_add_f32_e32 v67, v67, v141
	v_mul_f32_e32 v88, v88, v130
	s_waitcnt lgkmcnt(0)
; #define LAS __attribute__((address_space(3)))
; __device__ __forceinline__ void lru_gates(const Frame& F, LAS bf16_t* Wl, const LAS float* CT, LAS float* ucb, float (&av)[2][4][4], unsigned (&pw)[2][4][4]) {
;     ...
;             const f32x4 ba4 = *(const LAS f32x4*)(CT + (5 + 3 * d) * 64 + et * 16 + 4 * g), bx4 = *(const LAS f32x4*)(CT + (6 + 3 * d) * 64 + et * 16 + 4 * g), cs4 = *(const LAS f32x4*)(CT + (7 + 3 * d) * 64 + et * 16 + 4 * g);
;             const f32x4 u4 = *(const LAS f32x4*)(ucb + tk * 68 + et * 16 + 4 * g);
; #pragma unroll
;             for (int i = 0; i < 4; ++i) {
;                 const float r = sigmoidf_(ra[i] + ba4[i]), ig = sigmoidf_(ri[i] + bx4[i]);
;                 const float la = __uint_as_float(cvt_pk_bf16(cs4[i] * r, 0.f) << 16), a = __expf(la);
;                 av[d][et][i] = a; pw[d][et][i] = cvt_pk_bf16(la, __builtin_amdgcn_sqrtf(fmaxf(1.0f - a * a, 0.f)) * ig * u4[i]); }
;         }
; }
; template <int S> __device__ __forceinline__ void lru_step_f(float& a, float& x) { const float ap = dppf<0x110 + S>(1.0f, a), xp = dppf<0x110 + S>(0.0f, x); x = fmaf(a, xp, x); a = a * ap; }
; template <int S> __device__ __forceinline__ void lru_step_b(float& a, float& x) { const float ap = dppf<0x100 + S>(1.0f, a), xp = dppf<0x100 + S>(0.0f, x); x = fmaf(a, xp, x); a = a * ap; }
; __device__ __forceinline__ void ph_lru_a(const Frame& F, int jj) {
;     LAS bf16_t* Wl = (LAS bf16_t*)F.lds;
;     LAS float* ucb = (LAS float*)(F.lds + 36864 + F.wave * 4352);
;     LAS float* CT = (LAS float*)(F.lds + 36864 + 8 * 4352);
;     const bf16_t* wsrc = (const bf16_t*)(F.WB + WB_LRU);
;     float* AG = (float*)(F.R1 + R1_AG); bf16_t* GX = (bf16_t*)(F.R1 + R1_GX);
;     const float* cw = inp(F, 14) + (size_t)jj * 4 * 1024; const float* cb = inp(F, 15) + (size_t)jj * 1024;
;     const float* b_a = inp(F, 17) + (size_t)jj * 2 * 1024; const float* b_x = inp(F, 19) + (size_t)jj * 2 * 1024; const float* lam = inp(F, 20) + (size_t)jj * 2 * 1024;
;     const int tk = F.lane & 15, g = F.lane >> 4;
;     const int NTASK = NBAT * 16 * 11;
;     for (int task = F.wg; task < NTASK; task += F.G) {
;         const int grp = task % 11, kb = (task / 11) & 15, b = task / (11 * 16);
;         __syncthreads();
;         for (int i = F.tid; i < 4 * 4096 / 8; i += 512) { const int mg = i >> 9, r = i & 511;
	v_mul_f32_e32 v88, v146, v88
	v_cvt_pk_bf16_f32 v88, v64, v88
	v_add_f32_e32 v64, 1.0, v65
	v_rcp_f32_e32 v64, v64
	v_add_f32_e32 v65, v131, v89
	v_mul_f32_e32 v65, 0xbfb8aa3b, v65
	v_exp_f32_e32 v65, v65
	v_mul_f32_e32 v64, v135, v64
	v_cvt_pk_bf16_f32 v64, v64, v2
	v_mul_f32_e32 v67, 0xbfb8aa3b, v67
	v_lshlrev_b32_e32 v64, 16, v64
	v_mul_f32_e32 v89, 0x3fb8aa3b, v64
	v_exp_f32_e32 v130, v89
	v_add_f32_e32 v65, 1.0, v65
	v_rcp_f32_e32 v65, v65
	v_exp_f32_e32 v67, v67
	v_fma_f32 v89, -v130, v130, 1.0
	v_max_f32_e32 v89, 0, v89
	v_sqrt_f32_e32 v89, v89
	s_nop 0
	v_mul_f32_e32 v65, v65, v89
	v_mul_f32_e32 v65, v147, v65
	v_cvt_pk_bf16_f32 v89, v64, v65
	v_add_f32_e32 v64, 1.0, v66
	v_rcp_f32_e32 v64, v64
	v_add_f32_e32 v65, v132, v90
	v_mul_f32_e32 v65, 0xbfb8aa3b, v65
	v_exp_f32_e32 v65, v65
	v_mul_f32_e32 v64, v136, v64
	v_cvt_pk_bf16_f32 v64, v64, v2
	v_add_f32_e32 v65, 1.0, v65
	v_lshlrev_b32_e32 v64, 16, v64
	v_mul_f32_e32 v66, 0x3fb8aa3b, v64
	v_exp_f32_e32 v131, v66
	v_rcp_f32_e32 v65, v65
	v_fma_f32 v66, -v131, v131, 1.0
	v_max_f32_e32 v66, 0, v66
	v_sqrt_f32_e32 v66, v66
	s_nop 0
	v_mul_f32_e32 v65, v65, v66
	v_mul_f32_e32 v65, v148, v65
	v_cvt_pk_bf16_f32 v90, v64, v65
	v_add_f32_e32 v64, 1.0, v67
	v_rcp_f32_e32 v64, v64
	v_add_f32_e32 v65, v133, v91
	v_mul_f32_e32 v65, 0xbfb8aa3b, v65
	v_exp_f32_e32 v65, v65
	v_mul_f32_e32 v64, v137, v64
	v_cvt_pk_bf16_f32 v64, v64, v2
	v_add_f32_e32 v65, 1.0, v65
	v_lshlrev_b32_e32 v64, 16, v64
	v_mul_f32_e32 v66, 0x3fb8aa3b, v64
	v_exp_f32_e32 v132, v66
	v_rcp_f32_e32 v65, v65
	v_fma_f32 v66, -v132, v132, 1.0
	v_max_f32_e32 v66, 0, v66
	v_sqrt_f32_e32 v66, v66
	s_nop 0
	v_mul_f32_e32 v65, v65, v66
	v_mul_f32_e32 v65, v149, v65
	v_cvt_pk_bf16_f32 v91, v64, v65
	ds_read_b128 v[64:67], v114 offset:25344
	ds_read_b128 v[134:137], v114 offset:25408
	ds_read_b128 v[138:141], v114 offset:34560
	ds_read_b128 v[146:149], v114 offset:34624
	s_waitcnt lgkmcnt(3)
	v_mfma_f32_16x16x32_bf16 v[64:67], v[64:67], v[56:59], 0
	s_waitcnt lgkmcnt(1)
	v_mfma_f32_16x16x32_bf16 v[56:59], v[138:141], v[56:59], 0
	ds_read_b128 v[138:141], v115 offset:192
	v_mfma_f32_16x16x32_bf16 v[64:67], v[134:137], v[60:63], v[64:67]
	ds_read_b128 v[134:137], v116 offset:192
	s_waitcnt lgkmcnt(2)
	v_mfma_f32_16x16x32_bf16 v[56:59], v[146:149], v[60:63], v[56:59]
	ds_read_b128 v[60:63], v117 offset:192
	ds_read_b128 v[146:149], v120 offset:37056
	s_waitcnt lgkmcnt(3)
	s_nop 1
	v_add_f32_e32 v64, v64, v138
	v_mul_f32_e32 v64, 0xbfb8aa3b, v64
	v_exp_f32_e32 v64, v64
	s_waitcnt lgkmcnt(2)
	v_add_f32_e32 v56, v56, v134
	v_mul_f32_e32 v56, 0xbfb8aa3b, v56
	v_exp_f32_e32 v56, v56
	v_add_f32_e32 v64, 1.0, v64
	v_rcp_f32_e32 v64, v64
	v_add_f32_e32 v65, v65, v139
	v_add_f32_e32 v56, 1.0, v56
	v_rcp_f32_e32 v56, v56
	s_waitcnt lgkmcnt(1)
	v_mul_f32_e32 v60, v60, v64
	v_cvt_pk_bf16_f32 v60, v60, v2
	v_mul_f32_e32 v65, 0xbfb8aa3b, v65
	v_lshlrev_b32_e32 v60, 16, v60
	v_mul_f32_e32 v64, 0x3fb8aa3b, v60
	v_exp_f32_e32 v133, v64
	v_exp_f32_e32 v65, v65
	v_add_f32_e32 v57, v57, v135
	v_mul_f32_e32 v57, 0xbfb8aa3b, v57
	v_fma_f32 v64, -v133, v133, 1.0
	v_max_f32_e32 v64, 0, v64
	v_sqrt_f32_e32 v64, v64
	v_exp_f32_e32 v57, v57
	v_mul_f32_e32 v56, v56, v64
	s_waitcnt lgkmcnt(0)
	v_mul_f32_e32 v56, v146, v56
	v_cvt_pk_bf16_f32 v138, v60, v56
	v_add_f32_e32 v56, 1.0, v65
	v_rcp_f32_e32 v56, v56
	v_add_f32_e32 v57, 1.0, v57
	v_rcp_f32_e32 v57, v57
	v_and_b32_e32 v64, 0xffff0000, v52
	v_mul_f32_e32 v56, v61, v56
	v_cvt_pk_bf16_f32 v56, v56, v2
	v_add_f32_e32 v61, v66, v140
	v_lshlrev_b32_e32 v56, 16, v56
	v_mul_f32_e32 v60, 0x3fb8aa3b, v56
	v_exp_f32_e32 v134, v60
	v_mul_f32_e32 v61, 0xbfb8aa3b, v61
	v_exp_f32_e32 v61, v61
	v_and_b32_e32 v65, 0xffff0000, v53
	v_fma_f32 v60, -v134, v134, 1.0
	v_max_f32_e32 v60, 0, v60
	v_sqrt_f32_e32 v60, v60
	v_and_b32_e32 v66, 0xffff0000, v54
	v_mul_f32_e32 v57, v57, v60
	v_mul_f32_e32 v57, v147, v57
	v_cvt_pk_bf16_f32 v139, v56, v57
	v_add_f32_e32 v56, 1.0, v61
	v_rcp_f32_e32 v56, v56
	v_add_f32_e32 v57, v58, v136
	v_mul_f32_e32 v57, 0xbfb8aa3b, v57
	v_exp_f32_e32 v57, v57
	v_mul_f32_e32 v56, v62, v56
	v_cvt_pk_bf16_f32 v56, v56, v2
	v_add_f32_e32 v60, v67, v141
	v_lshlrev_b32_e32 v56, 16, v56
	v_mul_f32_e32 v58, 0x3fb8aa3b, v56
	v_exp_f32_e32 v135, v58
	v_add_f32_e32 v57, 1.0, v57
	v_rcp_f32_e32 v57, v57
	v_mul_f32_e32 v60, 0xbfb8aa3b, v60
	v_fma_f32 v58, -v135, v135, 1.0
	v_max_f32_e32 v58, 0, v58
	v_sqrt_f32_e32 v58, v58
	v_exp_f32_e32 v60, v60
	v_and_b32_e32 v67, 0xffff0000, v55
	v_and_b32_e32 v61, 0xffff0000, v69
	v_mul_f32_e32 v57, v57, v58
	v_mul_f32_e32 v57, v148, v57
	v_cvt_pk_bf16_f32 v140, v56, v57
	v_add_f32_e32 v56, 1.0, v60
	v_rcp_f32_e32 v56, v56
	v_add_f32_e32 v57, v59, v137
	v_mul_f32_e32 v57, 0xbfb8aa3b, v57
	v_exp_f32_e32 v57, v57
	v_mul_f32_e32 v56, v63, v56
	v_cvt_pk_bf16_f32 v56, v56, v2
	v_and_b32_e32 v60, 0xffff0000, v68
	v_lshlrev_b32_e32 v56, 16, v56
	v_mul_f32_e32 v58, 0x3fb8aa3b, v56
	v_exp_f32_e32 v136, v58
	v_add_f32_e32 v57, 1.0, v57
	v_rcp_f32_e32 v57, v57
	v_and_b32_e32 v62, 0xffff0000, v70
	v_fma_f32 v58, -v136, v136, 1.0
	v_max_f32_e32 v58, 0, v58
	v_sqrt_f32_e32 v58, v58
	v_and_b32_e32 v63, 0xffff0000, v71
	v_and_b32_e32 v59, 0xffff0000, v75
	v_mul_f32_e32 v57, v57, v58
	v_mul_f32_e32 v57, v149, v57
	v_cvt_pk_bf16_f32 v141, v56, v57
	v_add_u32_e32 v56, s8, v121
	v_ashrrev_i32_e32 v57, 31, v56
	v_lshlrev_b64 v[56:57], 13, v[56:57]
	v_lshl_add_u64 v[142:143], v[98:99], 0, v[56:57]
	global_store_dwordx4 v[142:143], v[52:55], off nt
	global_store_dwordx4 v[142:143], v[68:71], off offset:64 nt
	global_store_dwordx4 v[142:143], v[72:75], off offset:128 nt
; __device__ __forceinline__ void ph_lru_a(const Frame& F, int jj) {
;     ...
; #pragma unroll
;             for (int d = 0; d < 2; ++d)
; #pragma unroll
;                 for (int et = 0; et < 4; ++et) { u32x4 w; w.x = pw[d][et][0]; w.y = pw[d][et][1]; w.z = pw[d][et][2]; w.w = pw[d][et][3];
;                     __builtin_nontemporal_store(w, (u32x4*)(GX + (((size_t)row * 2 + d) * 1024 + kb * 64 + et * 16 + 4 * g) * 2));
; #pragma unroll
;                     for (int i = 0; i < 4; ++i) xv[d][et][i] = __uint_as_float(pw[d][et][i] & 0xffff0000u); }
;             LRU_SCANS(av, xv);
	global_store_dwordx4 v[142:143], v[76:79], off offset:192 nt
	v_add_co_u32_e32 v142, vcc, s97, v142
	v_and_b32_e32 v56, 0xffff0000, v72
	s_nop 0
	v_addc_co_u32_e32 v143, vcc, 0, v143, vcc
	v_and_b32_e32 v57, 0xffff0000, v73
	v_and_b32_e32 v58, 0xffff0000, v74
	v_and_b32_e32 v52, 0xffff0000, v76
	v_and_b32_e32 v53, 0xffff0000, v77
	v_and_b32_e32 v54, 0xffff0000, v78
	v_and_b32_e32 v55, 0xffff0000, v79
	global_store_dwordx4 v[142:143], v[80:83], off nt
	v_and_b32_e32 v68, 0xffff0000, v80
	v_and_b32_e32 v69, 0xffff0000, v81
	v_and_b32_e32 v70, 0xffff0000, v82
	v_and_b32_e32 v71, 0xffff0000, v83
	v_and_b32_e32 v72, 0xffff0000, v84
	v_and_b32_e32 v73, 0xffff0000, v85
	v_and_b32_e32 v74, 0xffff0000, v86
	v_and_b32_e32 v75, 0xffff0000, v87
	v_and_b32_e32 v76, 0xffff0000, v88
	v_and_b32_e32 v77, 0xffff0000, v89
	v_and_b32_e32 v78, 0xffff0000, v90
	v_and_b32_e32 v79, 0xffff0000, v91
	v_and_b32_e32 v80, 0xffff0000, v138
	v_and_b32_e32 v81, 0xffff0000, v139
	v_and_b32_e32 v82, 0xffff0000, v140
	v_and_b32_e32 v83, 0xffff0000, v141
	global_store_dwordx4 v[142:143], v[84:87], off offset:64 nt
	global_store_dwordx4 v[142:143], v[88:91], off offset:128 nt
	global_store_dwordx4 v[142:143], v[138:141], off offset:192 nt
	v_fmac_f32_dpp v64, v64, v36 row_shr:1 row_mask:0xf bank_mask:0xf
	v_fmac_f32_dpp v65, v65, v37 row_shr:1 row_mask:0xf bank_mask:0xf
	v_fmac_f32_dpp v66, v66, v38 row_shr:1 row_mask:0xf bank_mask:0xf
	v_fmac_f32_dpp v67, v67, v39 row_shr:1 row_mask:0xf bank_mask:0xf
	v_mul_f32_dpp v36, v36, v36 row_shr:1 row_mask:0xf bank_mask:0xf
	v_mul_f32_dpp v37, v37, v37 row_shr:1 row_mask:0xf bank_mask:0xf
	v_mul_f32_dpp v38, v38, v38 row_shr:1 row_mask:0xf bank_mask:0xf
	v_mul_f32_dpp v39, v39, v39 row_shr:1 row_mask:0xf bank_mask:0xf
	v_fmac_f32_dpp v68, v68, v103 row_shl:1 row_mask:0xf bank_mask:0xf
	v_fmac_f32_dpp v69, v69, v122 row_shl:1 row_mask:0xf bank_mask:0xf
	v_fmac_f32_dpp v70, v70, v123 row_shl:1 row_mask:0xf bank_mask:0xf
	v_fmac_f32_dpp v71, v71, v124 row_shl:1 row_mask:0xf bank_mask:0xf
	v_mul_f32_dpp v103, v103, v103 row_shl:1 row_mask:0xf bank_mask:0xf
	v_mul_f32_dpp v122, v122, v122 row_shl:1 row_mask:0xf bank_mask:0xf
	v_mul_f32_dpp v123, v123, v123 row_shl:1 row_mask:0xf bank_mask:0xf
	v_mul_f32_dpp v124, v124, v124 row_shl:1 row_mask:0xf bank_mask:0xf
	v_fmac_f32_dpp v60, v60, v40 row_shr:1 row_mask:0xf bank_mask:0xf
	v_fmac_f32_dpp v61, v61, v41 row_shr:1 row_mask:0xf bank_mask:0xf
	v_fmac_f32_dpp v62, v62, v42 row_shr:1 row_mask:0xf bank_mask:0xf
	v_fmac_f32_dpp v63, v63, v43 row_shr:1 row_mask:0xf bank_mask:0xf
	v_mul_f32_dpp v40, v40, v40 row_shr:1 row_mask:0xf bank_mask:0xf
	v_mul_f32_dpp v41, v41, v41 row_shr:1 row_mask:0xf bank_mask:0xf
	v_mul_f32_dpp v42, v42, v42 row_shr:1 row_mask:0xf bank_mask:0xf
	v_mul_f32_dpp v43, v43, v43 row_shr:1 row_mask:0xf bank_mask:0xf
	v_fmac_f32_dpp v72, v72, v125 row_shl:1 row_mask:0xf bank_mask:0xf
	v_fmac_f32_dpp v73, v73, v126 row_shl:1 row_mask:0xf bank_mask:0xf
	v_fmac_f32_dpp v74, v74, v127 row_shl:1 row_mask:0xf bank_mask:0xf
	v_fmac_f32_dpp v75, v75, v128 row_shl:1 row_mask:0xf bank_mask:0xf
	v_mul_f32_dpp v125, v125, v125 row_shl:1 row_mask:0xf bank_mask:0xf
	v_mul_f32_dpp v126, v126, v126 row_shl:1 row_mask:0xf bank_mask:0xf
	v_mul_f32_dpp v127, v127, v127 row_shl:1 row_mask:0xf bank_mask:0xf
	v_mul_f32_dpp v128, v128, v128 row_shl:1 row_mask:0xf bank_mask:0xf
	v_fmac_f32_dpp v56, v56, v44 row_shr:1 row_mask:0xf bank_mask:0xf
	v_fmac_f32_dpp v57, v57, v45 row_shr:1 row_mask:0xf bank_mask:0xf
	v_fmac_f32_dpp v58, v58, v46 row_shr:1 row_mask:0xf bank_mask:0xf
	v_fmac_f32_dpp v59, v59, v47 row_shr:1 row_mask:0xf bank_mask:0xf
	v_mul_f32_dpp v44, v44, v44 row_shr:1 row_mask:0xf bank_mask:0xf
	v_mul_f32_dpp v45, v45, v45 row_shr:1 row_mask:0xf bank_mask:0xf
	v_mul_f32_dpp v46, v46, v46 row_shr:1 row_mask:0xf bank_mask:0xf
	v_mul_f32_dpp v47, v47, v47 row_shr:1 row_mask:0xf bank_mask:0xf
	v_fmac_f32_dpp v76, v76, v129 row_shl:1 row_mask:0xf bank_mask:0xf
	v_fmac_f32_dpp v77, v77, v130 row_shl:1 row_mask:0xf bank_mask:0xf
	v_fmac_f32_dpp v78, v78, v131 row_shl:1 row_mask:0xf bank_mask:0xf
	v_fmac_f32_dpp v79, v79, v132 row_shl:1 row_mask:0xf bank_mask:0xf
	v_mul_f32_dpp v129, v129, v129 row_shl:1 row_mask:0xf bank_mask:0xf
	v_mul_f32_dpp v130, v130, v130 row_shl:1 row_mask:0xf bank_mask:0xf
	v_mul_f32_dpp v131, v131, v131 row_shl:1 row_mask:0xf bank_mask:0xf
	v_mul_f32_dpp v132, v132, v132 row_shl:1 row_mask:0xf bank_mask:0xf
	v_fmac_f32_dpp v52, v52, v48 row_shr:1 row_mask:0xf bank_mask:0xf
	v_fmac_f32_dpp v53, v53, v49 row_shr:1 row_mask:0xf bank_mask:0xf
	v_fmac_f32_dpp v54, v54, v50 row_shr:1 row_mask:0xf bank_mask:0xf
	v_fmac_f32_dpp v55, v55, v51 row_shr:1 row_mask:0xf bank_mask:0xf
	v_mul_f32_dpp v48, v48, v48 row_shr:1 row_mask:0xf bank_mask:0xf
	v_mul_f32_dpp v49, v49, v49 row_shr:1 row_mask:0xf bank_mask:0xf
	v_mul_f32_dpp v50, v50, v50 row_shr:1 row_mask:0xf bank_mask:0xf
	v_mul_f32_dpp v51, v51, v51 row_shr:1 row_mask:0xf bank_mask:0xf
	v_fmac_f32_dpp v80, v80, v133 row_shl:1 row_mask:0xf bank_mask:0xf
	v_fmac_f32_dpp v81, v81, v134 row_shl:1 row_mask:0xf bank_mask:0xf
	v_fmac_f32_dpp v82, v82, v135 row_shl:1 row_mask:0xf bank_mask:0xf
	v_fmac_f32_dpp v83, v83, v136 row_shl:1 row_mask:0xf bank_mask:0xf
	v_mul_f32_dpp v133, v133, v133 row_shl:1 row_mask:0xf bank_mask:0xf
	v_mul_f32_dpp v134, v134, v134 row_shl:1 row_mask:0xf bank_mask:0xf
	v_mul_f32_dpp v135, v135, v135 row_shl:1 row_mask:0xf bank_mask:0xf
	v_mul_f32_dpp v136, v136, v136 row_shl:1 row_mask:0xf bank_mask:0xf
	s_nop 0
	v_fmac_f32_dpp v64, v64, v36 row_shr:2 row_mask:0xf bank_mask:0xf
	v_fmac_f32_dpp v65, v65, v37 row_shr:2 row_mask:0xf bank_mask:0xf
	v_fmac_f32_dpp v66, v66, v38 row_shr:2 row_mask:0xf bank_mask:0xf
	v_fmac_f32_dpp v67, v67, v39 row_shr:2 row_mask:0xf bank_mask:0xf
	v_mul_f32_dpp v36, v36, v36 row_shr:2 row_mask:0xf bank_mask:0xf
	v_mul_f32_dpp v37, v37, v37 row_shr:2 row_mask:0xf bank_mask:0xf
	v_mul_f32_dpp v38, v38, v38 row_shr:2 row_mask:0xf bank_mask:0xf
	v_mul_f32_dpp v39, v39, v39 row_shr:2 row_mask:0xf bank_mask:0xf
	v_fmac_f32_dpp v68, v68, v103 row_shl:2 row_mask:0xf bank_mask:0xf
	v_fmac_f32_dpp v69, v69, v122 row_shl:2 row_mask:0xf bank_mask:0xf
	v_fmac_f32_dpp v70, v70, v123 row_shl:2 row_mask:0xf bank_mask:0xf
	v_fmac_f32_dpp v71, v71, v124 row_shl:2 row_mask:0xf bank_mask:0xf
	v_mul_f32_dpp v103, v103, v103 row_shl:2 row_mask:0xf bank_mask:0xf
	v_mul_f32_dpp v122, v122, v122 row_shl:2 row_mask:0xf bank_mask:0xf
	v_mul_f32_dpp v123, v123, v123 row_shl:2 row_mask:0xf bank_mask:0xf
	v_mul_f32_dpp v124, v124, v124 row_shl:2 row_mask:0xf bank_mask:0xf
	v_fmac_f32_dpp v60, v60, v40 row_shr:2 row_mask:0xf bank_mask:0xf
	v_fmac_f32_dpp v61, v61, v41 row_shr:2 row_mask:0xf bank_mask:0xf
	v_fmac_f32_dpp v62, v62, v42 row_shr:2 row_mask:0xf bank_mask:0xf
	v_fmac_f32_dpp v63, v63, v43 row_shr:2 row_mask:0xf bank_mask:0xf
	v_mul_f32_dpp v40, v40, v40 row_shr:2 row_mask:0xf bank_mask:0xf
	v_mul_f32_dpp v41, v41, v41 row_shr:2 row_mask:0xf bank_mask:0xf
	v_mul_f32_dpp v42, v42, v42 row_shr:2 row_mask:0xf bank_mask:0xf
	v_mul_f32_dpp v43, v43, v43 row_shr:2 row_mask:0xf bank_mask:0xf
	v_fmac_f32_dpp v72, v72, v125 row_shl:2 row_mask:0xf bank_mask:0xf
	v_fmac_f32_dpp v73, v73, v126 row_shl:2 row_mask:0xf bank_mask:0xf
	v_fmac_f32_dpp v74, v74, v127 row_shl:2 row_mask:0xf bank_mask:0xf
	v_fmac_f32_dpp v75, v75, v128 row_shl:2 row_mask:0xf bank_mask:0xf
	v_mul_f32_dpp v125, v125, v125 row_shl:2 row_mask:0xf bank_mask:0xf
	v_mul_f32_dpp v126, v126, v126 row_shl:2 row_mask:0xf bank_mask:0xf
	v_mul_f32_dpp v127, v127, v127 row_shl:2 row_mask:0xf bank_mask:0xf
	v_mul_f32_dpp v128, v128, v128 row_shl:2 row_mask:0xf bank_mask:0xf
	v_fmac_f32_dpp v56, v56, v44 row_shr:2 row_mask:0xf bank_mask:0xf
	v_fmac_f32_dpp v57, v57, v45 row_shr:2 row_mask:0xf bank_mask:0xf
	v_fmac_f32_dpp v58, v58, v46 row_shr:2 row_mask:0xf bank_mask:0xf
	v_fmac_f32_dpp v59, v59, v47 row_shr:2 row_mask:0xf bank_mask:0xf
	v_mul_f32_dpp v44, v44, v44 row_shr:2 row_mask:0xf bank_mask:0xf
	v_mul_f32_dpp v45, v45, v45 row_shr:2 row_mask:0xf bank_mask:0xf
	v_mul_f32_dpp v46, v46, v46 row_shr:2 row_mask:0xf bank_mask:0xf
	v_mul_f32_dpp v47, v47, v47 row_shr:2 row_mask:0xf bank_mask:0xf
	v_fmac_f32_dpp v76, v76, v129 row_shl:2 row_mask:0xf bank_mask:0xf
	v_fmac_f32_dpp v77, v77, v130 row_shl:2 row_mask:0xf bank_mask:0xf
	v_fmac_f32_dpp v78, v78, v131 row_shl:2 row_mask:0xf bank_mask:0xf
	v_fmac_f32_dpp v79, v79, v132 row_shl:2 row_mask:0xf bank_mask:0xf
	v_mul_f32_dpp v129, v129, v129 row_shl:2 row_mask:0xf bank_mask:0xf
	v_mul_f32_dpp v130, v130, v130 row_shl:2 row_mask:0xf bank_mask:0xf
	v_mul_f32_dpp v131, v131, v131 row_shl:2 row_mask:0xf bank_mask:0xf
	v_mul_f32_dpp v132, v132, v132 row_shl:2 row_mask:0xf bank_mask:0xf
	v_fmac_f32_dpp v52, v52, v48 row_shr:2 row_mask:0xf bank_mask:0xf
	v_fmac_f32_dpp v53, v53, v49 row_shr:2 row_mask:0xf bank_mask:0xf
	v_fmac_f32_dpp v54, v54, v50 row_shr:2 row_mask:0xf bank_mask:0xf
	v_fmac_f32_dpp v55, v55, v51 row_shr:2 row_mask:0xf bank_mask:0xf
	v_mul_f32_dpp v48, v48, v48 row_shr:2 row_mask:0xf bank_mask:0xf
	v_mul_f32_dpp v49, v49, v49 row_shr:2 row_mask:0xf bank_mask:0xf
	v_mul_f32_dpp v50, v50, v50 row_shr:2 row_mask:0xf bank_mask:0xf
	v_mul_f32_dpp v51, v51, v51 row_shr:2 row_mask:0xf bank_mask:0xf
	v_fmac_f32_dpp v80, v80, v133 row_shl:2 row_mask:0xf bank_mask:0xf
	v_fmac_f32_dpp v81, v81, v134 row_shl:2 row_mask:0xf bank_mask:0xf
	v_fmac_f32_dpp v82, v82, v135 row_shl:2 row_mask:0xf bank_mask:0xf
	v_fmac_f32_dpp v83, v83, v136 row_shl:2 row_mask:0xf bank_mask:0xf
	v_mul_f32_dpp v133, v133, v133 row_shl:2 row_mask:0xf bank_mask:0xf
	v_mul_f32_dpp v134, v134, v134 row_shl:2 row_mask:0xf bank_mask:0xf
	v_mul_f32_dpp v135, v135, v135 row_shl:2 row_mask:0xf bank_mask:0xf
	v_mul_f32_dpp v136, v136, v136 row_shl:2 row_mask:0xf bank_mask:0xf
	s_nop 0
	v_fmac_f32_dpp v64, v64, v36 row_shr:4 row_mask:0xf bank_mask:0xf
	v_fmac_f32_dpp v65, v65, v37 row_shr:4 row_mask:0xf bank_mask:0xf
	v_fmac_f32_dpp v66, v66, v38 row_shr:4 row_mask:0xf bank_mask:0xf
	v_fmac_f32_dpp v67, v67, v39 row_shr:4 row_mask:0xf bank_mask:0xf
	v_mul_f32_dpp v36, v36, v36 row_shr:4 row_mask:0xf bank_mask:0xf
	v_mul_f32_dpp v37, v37, v37 row_shr:4 row_mask:0xf bank_mask:0xf
	v_mul_f32_dpp v38, v38, v38 row_shr:4 row_mask:0xf bank_mask:0xf
	v_mul_f32_dpp v39, v39, v39 row_shr:4 row_mask:0xf bank_mask:0xf
	v_fmac_f32_dpp v68, v68, v103 row_shl:4 row_mask:0xf bank_mask:0xf
	v_fmac_f32_dpp v69, v69, v122 row_shl:4 row_mask:0xf bank_mask:0xf
	v_fmac_f32_dpp v70, v70, v123 row_shl:4 row_mask:0xf bank_mask:0xf
	v_fmac_f32_dpp v71, v71, v124 row_shl:4 row_mask:0xf bank_mask:0xf
	v_mul_f32_dpp v103, v103, v103 row_shl:4 row_mask:0xf bank_mask:0xf
	v_mul_f32_dpp v122, v122, v122 row_shl:4 row_mask:0xf bank_mask:0xf
	v_mul_f32_dpp v123, v123, v123 row_shl:4 row_mask:0xf bank_mask:0xf
	v_mul_f32_dpp v124, v124, v124 row_shl:4 row_mask:0xf bank_mask:0xf
	v_fmac_f32_dpp v60, v60, v40 row_shr:4 row_mask:0xf bank_mask:0xf
	v_fmac_f32_dpp v61, v61, v41 row_shr:4 row_mask:0xf bank_mask:0xf
	v_fmac_f32_dpp v62, v62, v42 row_shr:4 row_mask:0xf bank_mask:0xf
	v_fmac_f32_dpp v63, v63, v43 row_shr:4 row_mask:0xf bank_mask:0xf
; __device__ __forceinline__ void ph_lru_a(const Frame& F, int jj) {
;     ...
; #pragma unroll
;             for (int d = 0; d < 2; ++d) if (tk == (d ? 0 : 15)) {
	v_mul_f32_dpp v40, v40, v40 row_shr:4 row_mask:0xf bank_mask:0xf
	v_mul_f32_dpp v41, v41, v41 row_shr:4 row_mask:0xf bank_mask:0xf
	v_mul_f32_dpp v42, v42, v42 row_shr:4 row_mask:0xf bank_mask:0xf
	v_mul_f32_dpp v43, v43, v43 row_shr:4 row_mask:0xf bank_mask:0xf
	v_fmac_f32_dpp v72, v72, v125 row_shl:4 row_mask:0xf bank_mask:0xf
	v_fmac_f32_dpp v73, v73, v126 row_shl:4 row_mask:0xf bank_mask:0xf
	v_fmac_f32_dpp v74, v74, v127 row_shl:4 row_mask:0xf bank_mask:0xf
	v_fmac_f32_dpp v75, v75, v128 row_shl:4 row_mask:0xf bank_mask:0xf
	v_mul_f32_dpp v125, v125, v125 row_shl:4 row_mask:0xf bank_mask:0xf
	v_mul_f32_dpp v126, v126, v126 row_shl:4 row_mask:0xf bank_mask:0xf
	v_mul_f32_dpp v127, v127, v127 row_shl:4 row_mask:0xf bank_mask:0xf
	v_mul_f32_dpp v128, v128, v128 row_shl:4 row_mask:0xf bank_mask:0xf
	v_fmac_f32_dpp v56, v56, v44 row_shr:4 row_mask:0xf bank_mask:0xf
	v_fmac_f32_dpp v57, v57, v45 row_shr:4 row_mask:0xf bank_mask:0xf
	v_fmac_f32_dpp v58, v58, v46 row_shr:4 row_mask:0xf bank_mask:0xf
	v_fmac_f32_dpp v59, v59, v47 row_shr:4 row_mask:0xf bank_mask:0xf
	v_mul_f32_dpp v44, v44, v44 row_shr:4 row_mask:0xf bank_mask:0xf
	v_mul_f32_dpp v45, v45, v45 row_shr:4 row_mask:0xf bank_mask:0xf
	v_mul_f32_dpp v46, v46, v46 row_shr:4 row_mask:0xf bank_mask:0xf
	v_mul_f32_dpp v47, v47, v47 row_shr:4 row_mask:0xf bank_mask:0xf
	v_fmac_f32_dpp v76, v76, v129 row_shl:4 row_mask:0xf bank_mask:0xf
	v_fmac_f32_dpp v77, v77, v130 row_shl:4 row_mask:0xf bank_mask:0xf
	v_fmac_f32_dpp v78, v78, v131 row_shl:4 row_mask:0xf bank_mask:0xf
	v_fmac_f32_dpp v79, v79, v132 row_shl:4 row_mask:0xf bank_mask:0xf
	v_mul_f32_dpp v129, v129, v129 row_shl:4 row_mask:0xf bank_mask:0xf
	v_mul_f32_dpp v130, v130, v130 row_shl:4 row_mask:0xf bank_mask:0xf
	v_mul_f32_dpp v131, v131, v131 row_shl:4 row_mask:0xf bank_mask:0xf
	v_mul_f32_dpp v132, v132, v132 row_shl:4 row_mask:0xf bank_mask:0xf
	v_fmac_f32_dpp v52, v52, v48 row_shr:4 row_mask:0xf bank_mask:0xf
	v_fmac_f32_dpp v53, v53, v49 row_shr:4 row_mask:0xf bank_mask:0xf
	v_fmac_f32_dpp v54, v54, v50 row_shr:4 row_mask:0xf bank_mask:0xf
	v_fmac_f32_dpp v55, v55, v51 row_shr:4 row_mask:0xf bank_mask:0xf
	v_mul_f32_dpp v48, v48, v48 row_shr:4 row_mask:0xf bank_mask:0xf
	v_mul_f32_dpp v49, v49, v49 row_shr:4 row_mask:0xf bank_mask:0xf
	v_mul_f32_dpp v50, v50, v50 row_shr:4 row_mask:0xf bank_mask:0xf
	v_mul_f32_dpp v51, v51, v51 row_shr:4 row_mask:0xf bank_mask:0xf
	v_fmac_f32_dpp v80, v80, v133 row_shl:4 row_mask:0xf bank_mask:0xf
	v_fmac_f32_dpp v81, v81, v134 row_shl:4 row_mask:0xf bank_mask:0xf
	v_fmac_f32_dpp v82, v82, v135 row_shl:4 row_mask:0xf bank_mask:0xf
	v_fmac_f32_dpp v83, v83, v136 row_shl:4 row_mask:0xf bank_mask:0xf
	v_mul_f32_dpp v133, v133, v133 row_shl:4 row_mask:0xf bank_mask:0xf
	v_mul_f32_dpp v134, v134, v134 row_shl:4 row_mask:0xf bank_mask:0xf
	v_mul_f32_dpp v135, v135, v135 row_shl:4 row_mask:0xf bank_mask:0xf
	v_mul_f32_dpp v136, v136, v136 row_shl:4 row_mask:0xf bank_mask:0xf
	v_cmp_lt_i32_e32 vcc, 14, v104
	s_mov_b64 s[8:9], 0
	v_fmac_f32_dpp v64, v64, v36 row_shr:8 row_mask:0xf bank_mask:0xf
	v_fmac_f32_dpp v65, v65, v37 row_shr:8 row_mask:0xf bank_mask:0xf
	v_fmac_f32_dpp v66, v66, v38 row_shr:8 row_mask:0xf bank_mask:0xf
	v_fmac_f32_dpp v67, v67, v39 row_shr:8 row_mask:0xf bank_mask:0xf
	v_mul_f32_dpp v36, v36, v36 row_shr:8 row_mask:0xf bank_mask:0xf
	v_mul_f32_dpp v37, v37, v37 row_shr:8 row_mask:0xf bank_mask:0xf
	v_mul_f32_dpp v38, v38, v38 row_shr:8 row_mask:0xf bank_mask:0xf
	v_mul_f32_dpp v39, v39, v39 row_shr:8 row_mask:0xf bank_mask:0xf
	v_fmac_f32_dpp v68, v68, v103 row_shl:8 row_mask:0xf bank_mask:0xf
	v_fmac_f32_dpp v69, v69, v122 row_shl:8 row_mask:0xf bank_mask:0xf
	v_fmac_f32_dpp v70, v70, v123 row_shl:8 row_mask:0xf bank_mask:0xf
; __device__ __forceinline__ void ph_lru_a(const Frame& F, int jj) {
;     ...
; #pragma unroll
;             for (int d = 0; d < 2; ++d) if (tk == (d ? 0 : 15)) {
;                 float* ag = AG + (((size_t)(b * 2 + d) * LRU_NT + nt) * 2) * 1024 + kb * 64;
; #pragma unroll
;                 for (int et = 0; et < 4; ++et) { *(f32x4*)(ag + et * 16 + 4 * g) = (f32x4){av[d][et][0], av[d][et][1], av[d][et][2], av[d][et][3]};
;                     *(f32x4*)(ag + 1024 + et * 16 + 4 * g) = (f32x4){xv[d][et][0], xv[d][et][1], xv[d][et][2], xv[d][et][3]}; }
;             }
	v_fmac_f32_dpp v71, v71, v124 row_shl:8 row_mask:0xf bank_mask:0xf
	v_mul_f32_dpp v103, v103, v103 row_shl:8 row_mask:0xf bank_mask:0xf
	v_mul_f32_dpp v122, v122, v122 row_shl:8 row_mask:0xf bank_mask:0xf
	v_mul_f32_dpp v123, v123, v123 row_shl:8 row_mask:0xf bank_mask:0xf
	v_mul_f32_dpp v124, v124, v124 row_shl:8 row_mask:0xf bank_mask:0xf
	v_fmac_f32_dpp v60, v60, v40 row_shr:8 row_mask:0xf bank_mask:0xf
	v_fmac_f32_dpp v61, v61, v41 row_shr:8 row_mask:0xf bank_mask:0xf
	v_fmac_f32_dpp v62, v62, v42 row_shr:8 row_mask:0xf bank_mask:0xf
	v_fmac_f32_dpp v63, v63, v43 row_shr:8 row_mask:0xf bank_mask:0xf
	v_mul_f32_dpp v40, v40, v40 row_shr:8 row_mask:0xf bank_mask:0xf
	v_mul_f32_dpp v41, v41, v41 row_shr:8 row_mask:0xf bank_mask:0xf
	v_mul_f32_dpp v42, v42, v42 row_shr:8 row_mask:0xf bank_mask:0xf
	v_mul_f32_dpp v43, v43, v43 row_shr:8 row_mask:0xf bank_mask:0xf
	v_fmac_f32_dpp v72, v72, v125 row_shl:8 row_mask:0xf bank_mask:0xf
	v_fmac_f32_dpp v73, v73, v126 row_shl:8 row_mask:0xf bank_mask:0xf
	v_fmac_f32_dpp v74, v74, v127 row_shl:8 row_mask:0xf bank_mask:0xf
	v_fmac_f32_dpp v75, v75, v128 row_shl:8 row_mask:0xf bank_mask:0xf
	v_mul_f32_dpp v125, v125, v125 row_shl:8 row_mask:0xf bank_mask:0xf
	v_mul_f32_dpp v126, v126, v126 row_shl:8 row_mask:0xf bank_mask:0xf
	v_mul_f32_dpp v127, v127, v127 row_shl:8 row_mask:0xf bank_mask:0xf
	v_mul_f32_dpp v128, v128, v128 row_shl:8 row_mask:0xf bank_mask:0xf
	v_fmac_f32_dpp v56, v56, v44 row_shr:8 row_mask:0xf bank_mask:0xf
	v_fmac_f32_dpp v57, v57, v45 row_shr:8 row_mask:0xf bank_mask:0xf
	v_fmac_f32_dpp v58, v58, v46 row_shr:8 row_mask:0xf bank_mask:0xf
	v_fmac_f32_dpp v59, v59, v47 row_shr:8 row_mask:0xf bank_mask:0xf
	v_mul_f32_dpp v44, v44, v44 row_shr:8 row_mask:0xf bank_mask:0xf
	v_mul_f32_dpp v45, v45, v45 row_shr:8 row_mask:0xf bank_mask:0xf
	v_mul_f32_dpp v46, v46, v46 row_shr:8 row_mask:0xf bank_mask:0xf
	v_mul_f32_dpp v47, v47, v47 row_shr:8 row_mask:0xf bank_mask:0xf
	v_fmac_f32_dpp v76, v76, v129 row_shl:8 row_mask:0xf bank_mask:0xf
	v_fmac_f32_dpp v77, v77, v130 row_shl:8 row_mask:0xf bank_mask:0xf
	v_fmac_f32_dpp v78, v78, v131 row_shl:8 row_mask:0xf bank_mask:0xf
	v_fmac_f32_dpp v79, v79, v132 row_shl:8 row_mask:0xf bank_mask:0xf
	v_mul_f32_dpp v129, v129, v129 row_shl:8 row_mask:0xf bank_mask:0xf
	v_mul_f32_dpp v130, v130, v130 row_shl:8 row_mask:0xf bank_mask:0xf
	v_mul_f32_dpp v131, v131, v131 row_shl:8 row_mask:0xf bank_mask:0xf
	v_mul_f32_dpp v132, v132, v132 row_shl:8 row_mask:0xf bank_mask:0xf
	v_fmac_f32_dpp v52, v52, v48 row_shr:8 row_mask:0xf bank_mask:0xf
	v_fmac_f32_dpp v53, v53, v49 row_shr:8 row_mask:0xf bank_mask:0xf
	v_fmac_f32_dpp v54, v54, v50 row_shr:8 row_mask:0xf bank_mask:0xf
	v_fmac_f32_dpp v55, v55, v51 row_shr:8 row_mask:0xf bank_mask:0xf
	v_mul_f32_dpp v48, v48, v48 row_shr:8 row_mask:0xf bank_mask:0xf
	v_mul_f32_dpp v49, v49, v49 row_shr:8 row_mask:0xf bank_mask:0xf
	v_mul_f32_dpp v50, v50, v50 row_shr:8 row_mask:0xf bank_mask:0xf
	v_mul_f32_dpp v51, v51, v51 row_shr:8 row_mask:0xf bank_mask:0xf
	v_fmac_f32_dpp v80, v80, v133 row_shl:8 row_mask:0xf bank_mask:0xf
	v_fmac_f32_dpp v81, v81, v134 row_shl:8 row_mask:0xf bank_mask:0xf
	v_fmac_f32_dpp v82, v82, v135 row_shl:8 row_mask:0xf bank_mask:0xf
	v_fmac_f32_dpp v83, v83, v136 row_shl:8 row_mask:0xf bank_mask:0xf
	v_mul_f32_dpp v133, v133, v133 row_shl:8 row_mask:0xf bank_mask:0xf
	v_mul_f32_dpp v134, v134, v134 row_shl:8 row_mask:0xf bank_mask:0xf
	v_mul_f32_dpp v135, v135, v135 row_shl:8 row_mask:0xf bank_mask:0xf
	v_mul_f32_dpp v136, v136, v136 row_shl:8 row_mask:0xf bank_mask:0xf
	s_and_saveexec_b64 s[20:21], vcc
	s_xor_b64 s[24:25], exec, s[20:21]
	s_cbranch_execz .LBB0_469
	s_mov_b64 s[8:9], exec
	s_or_saveexec_b64 s[24:25], s[24:25]
	v_mov_b32_e32 v84, s26
	s_xor_b64 exec, exec, s[24:25]
	s_cbranch_execnz .LBB0_470
